# adds hand-scheduled NA unit body with per-wave start stagger and streamlined GEMM2 scatter epilogue on top of the one-token-per-lane routing
# baseline (speedup 1.0000x reference)
; #define LAS __attribute__((address_space(3)))
; __device__ __forceinline__ const char* uni_ptr(const char* p) { const unsigned long long v = (unsigned long long)p; const unsigned lo = __builtin_amdgcn_readfirstlane((unsigned)v), hi = __builtin_amdgcn_readfirstlane((unsigned)(v >> 32)); return (const char*)(((unsigned long long)hi << 32) | lo); }
; #define NA_SB() __builtin_amdgcn_sched_barrier(0)
; #define NA_WLOAD(vb_, cw) do { _Pragma("unroll") for (int d = 0; d < 4; ++d) vb_[d] = gld16o(vbase + ((size_t)(d * 16) * SPB + (cw) * 64) * 2, vlo); } while (0)
; template <bool WIN>
; __device__ __forceinline__ void na_unit(Frame& F, int b, int h, int r, int strip) {
;     ...
;     int ln_ = F.lane; asm volatile("" : "+v"(ln_));
;     const int i = ln_ & 15, g = ln_ >> 4;
;     const int qrow0 = WIN ? (b * SEQ + r * 64 + strip * 16) : (NLAT + b * CTXL + strip * 16);
;     const int ki = 8 * (i >> 2) + (i & 3);
;     const unsigned qlo = (unsigned)((i * DIN + 8 * g) * 2), klo = (unsigned)((ki * DIN + 8 * g) * 2), vlo = (unsigned)((i * SPB + 8 * g) * 2);
;     const char* qb = uni_ptr((const char*)(U + (size_t)qrow0 * DIN + UQ + h * 64));
;     const bf16x8 q0 = gld16o(qb, qlo), q1 = gld16o(qb + 64, qlo);
;     int kr0 = 0, u0 = 0;
;     if (WIN) { kr0 = r - 4; kr0 = kr0 < 0 ? 0 : (kr0 > 56 ? 56 : kr0); u0 = strip == 0 ? 0 : (strip == 1 ? 8 : (strip == 2 ? 24 : 32)); }
;     const LAS bf16_t* KR = (const LAS bf16_t*)(F.lds + NA_KR);
;     const char* vbase = uni_ptr((const char*)(VT + kr0 * 64 + u0));
;     f32x4 o[4];
; #pragma unroll
;     for (int d = 0; d < 4; ++d) o[d] = (f32x4){0.f, 0.f, 0.f, 0.f};
;     float lsum = 0.f;
;     ...
;     bf16x8 vA[4], vB[4], vC[4];
;     if (WIN) { NA_WLOAD(vA, 0); NA_WLOAD(vB, 1); NA_WLOAD(vC, 2); NA_SB(); }
;     ...
;     if (WIN) {
;         const int c = strip * 16 + i; int kc0 = c - 8; kc0 = kc0 < 0 ? 0 : (kc0 > 48 ? 48 : kc0);
;         int dcl[2][4]; bool okm[2][4];
; #pragma unroll
;         for (int t = 0; t < 2; ++t)
; #pragma unroll
;             for (int e = 0; e < 4; ++e) { const int kc = u0 + 8 * g + 4 * t + e; okm[t][e] = (kc >= kc0) && (kc < kc0 + 16); int dc = kc - c + 15; dcl[t][e] = okm[t][e] ? (dc < 0 ? 0 : (dc > 30 ? 30 : dc)) : 31; }
.LBB0_491:
	s_andn2_b64 vcc, exec, s[2:3]
	s_mov_b32 s2, s61
	s_cbranch_vccnz .LBB0_493
	s_mov_b32 s2, 8
.LBB0_493:
	s_mov_b32 s0, s97
.Lna_stag_loop:
	s_cmp_eq_u32 s0, 0
	s_cbranch_scc1 .Lna_nostag
	s_sleep 2
	s_sub_u32 s0, s0, 1
	s_branch .Lna_stag_loop
.Lna_nostag:
	s_sub_i32 s3, s76, 4
	s_max_i32 s3, s3, 0
	s_min_i32 s3, s3, 56
	s_mov_b32 s18, 0x42ad1f97
	s_mov_b32 s20, s79
	s_mov_b32 s21, s80
	v_lshrrev_b32_e32 v225, 2, v98
	v_and_b32_e32 v236, 3, v98
	v_lshl_or_b32 v225, v225, 3, v236
	v_lshlrev_b32_e32 v237, 1, v99
	s_movk_i32 s4, 0x90
	s_movk_i32 s5, 0x210
	s_movk_i32 s8, 0x2200
	v_mad_u32_u24 v200, v225, s4, v237
	v_add_u32_e32 v200, 0x800, v200
	v_mad_u32_u24 v201, v98, s5, v237
	v_add_u32_e32 v201, 0x9800, v201
	ds_read_b128 v[44:47], v200 offset:0
	ds_read_b128 v[48:51], v200 offset:64
	ds_read_b128 v[52:55], v200 offset:576
	ds_read_b128 v[56:59], v200 offset:640
	ds_read_b128 v[60:63], v201 offset:0
	ds_read_b128 v[64:67], v201 offset:8448
	ds_read_b128 v[68:71], v201 offset:16896
	ds_read_b128 v[72:75], v201 offset:25344
	s_lshl_b32 s0, s3, 6
	s_add_i32 s0, s0, s2
	s_lshl_b32 s0, s0, 1
	v_mad_u32_u24 v204, v98, s8, v237
	v_add_u32_e32 v204, s0, v204
	v_add_u32_e32 v205, 0x22000, v204
	v_add_u32_e32 v206, 0x44000, v204
	v_add_u32_e32 v207, 0x66000, v204
	global_load_dwordx4 v[104:107], v204, s[20:21] offset:0
	global_load_dwordx4 v[108:111], v205, s[20:21] offset:0
	global_load_dwordx4 v[112:115], v206, s[20:21] offset:0
	global_load_dwordx4 v[116:119], v207, s[20:21] offset:0
	global_load_dwordx4 v[120:123], v204, s[20:21] offset:128
	global_load_dwordx4 v[124:127], v205, s[20:21] offset:128
	global_load_dwordx4 v[128:131], v206, s[20:21] offset:128
	global_load_dwordx4 v[132:135], v207, s[20:21] offset:128
	global_load_dwordx4 v[156:159], v204, s[20:21] offset:256
	global_load_dwordx4 v[160:163], v205, s[20:21] offset:256
	global_load_dwordx4 v[164:167], v206, s[20:21] offset:256
	global_load_dwordx4 v[168:171], v207, s[20:21] offset:256
	global_load_dwordx4 v[172:175], v204, s[20:21] offset:384
	global_load_dwordx4 v[176:179], v205, s[20:21] offset:384
	global_load_dwordx4 v[180:183], v206, s[20:21] offset:384
	global_load_dwordx4 v[184:187], v207, s[20:21] offset:384
	s_mul_i32 s0, s2, 0x90
	s_add_i32 s0, s0, 0x11400
	v_add_u32_e32 v202, s0, v200
	s_sub_i32 s9, s3, s76
	s_add_i32 s9, s9, 7
	s_lshl_b32 s9, s9, 7
	s_lshl_b32 s0, s59, 4
	v_add_u32_e32 v238, s0, v98
	v_add_u32_e32 v239, -8, v238
	v_med3_i32 v239, v239, 0, 48
	v_add_u32_e32 v240, s2, v99
	v_mov_b32_e32 v244, 31
	v_add_u32_e32 v241, 0, v240
	v_sub_u32_e32 v242, v241, v239
	v_sub_u32_e32 v243, v241, v238
	v_cmp_gt_u32_e32 vcc, 16, v242
	v_add_u32_e32 v243, 15, v243
	v_med3_i32 v243, v243, 0, 30
	v_cndmask_b32_e32 v243, v244, v243, vcc
	v_lshl_add_u32 v216, v243, 2, s9
	v_add_u32_e32 v241, 1, v240
	v_sub_u32_e32 v242, v241, v239
	v_sub_u32_e32 v243, v241, v238
	v_cmp_gt_u32_e32 vcc, 16, v242
	v_add_u32_e32 v243, 15, v243
	v_med3_i32 v243, v243, 0, 30
	v_cndmask_b32_e32 v243, v244, v243, vcc
	v_lshl_add_u32 v217, v243, 2, s9
	v_add_u32_e32 v241, 2, v240
	v_sub_u32_e32 v242, v241, v239
	v_sub_u32_e32 v243, v241, v238
	v_cmp_gt_u32_e32 vcc, 16, v242
	v_add_u32_e32 v243, 15, v243
	v_med3_i32 v243, v243, 0, 30
	v_cndmask_b32_e32 v243, v244, v243, vcc
	v_lshl_add_u32 v218, v243, 2, s9
	v_add_u32_e32 v241, 3, v240
	v_sub_u32_e32 v242, v241, v239
	v_sub_u32_e32 v243, v241, v238
	v_cmp_gt_u32_e32 vcc, 16, v242
	v_add_u32_e32 v243, 15, v243
	v_med3_i32 v243, v243, 0, 30
	v_cndmask_b32_e32 v243, v244, v243, vcc
	v_lshl_add_u32 v219, v243, 2, s9
	v_add_u32_e32 v241, 4, v240
	v_sub_u32_e32 v242, v241, v239
	v_sub_u32_e32 v243, v241, v238
	v_cmp_gt_u32_e32 vcc, 16, v242
	v_add_u32_e32 v243, 15, v243
	v_med3_i32 v243, v243, 0, 30
	v_cndmask_b32_e32 v243, v244, v243, vcc
	v_lshl_add_u32 v220, v243, 2, s9
	v_add_u32_e32 v241, 5, v240
	v_sub_u32_e32 v242, v241, v239
	v_sub_u32_e32 v243, v241, v238
	v_cmp_gt_u32_e32 vcc, 16, v242
	v_add_u32_e32 v243, 15, v243
	v_med3_i32 v243, v243, 0, 30
	v_cndmask_b32_e32 v243, v244, v243, vcc
	v_lshl_add_u32 v221, v243, 2, s9
	v_add_u32_e32 v241, 6, v240
	v_sub_u32_e32 v242, v241, v239
	v_sub_u32_e32 v243, v241, v238
	v_cmp_gt_u32_e32 vcc, 16, v242
	v_add_u32_e32 v243, 15, v243
	v_med3_i32 v243, v243, 0, 30
	v_cndmask_b32_e32 v243, v244, v243, vcc
	v_lshl_add_u32 v222, v243, 2, s9
	v_add_u32_e32 v241, 7, v240
	v_sub_u32_e32 v242, v241, v239
	v_sub_u32_e32 v243, v241, v238
	v_cmp_gt_u32_e32 vcc, 16, v242
	v_add_u32_e32 v243, 15, v243
	v_med3_i32 v243, v243, 0, 30
	v_cndmask_b32_e32 v243, v244, v243, vcc
	v_lshl_add_u32 v223, v243, 2, s9
	v_lshl_add_u32 v224, v98, 11, v99
	s_lshl_b32 s0, s48, 11
	s_add_u32 s10, s81, s0
	s_addc_u32 s11, s82, 0
	v_lshlrev_b32_e32 v246, 2, v100
	v_xor_b32_e32 v247, 0x80, v246
	v_xor_b32_e32 v246, 64, v246
	v_mov_b32_e32 v16, 0
	v_mov_b32_e32 v17, 0
	v_mov_b32_e32 v18, 0
	v_mov_b32_e32 v19, 0
	v_mov_b32_e32 v20, 0
	v_mov_b32_e32 v21, 0
	v_mov_b32_e32 v22, 0
	v_mov_b32_e32 v23, 0
	v_mov_b32_e32 v24, 0
	v_mov_b32_e32 v25, 0
	v_mov_b32_e32 v26, 0
	v_mov_b32_e32 v27, 0
	v_mov_b32_e32 v28, 0
	v_mov_b32_e32 v29, 0
	v_mov_b32_e32 v30, 0
	v_mov_b32_e32 v31, 0
	v_mov_b32_e32 v198, 0
	v_mov_b32_e32 v199, 0
	s_mul_i32 s0, s3, 57
	s_bfe_u32 s0, s0, 0x70009
	s_mul_i32 s0, s0, 9
	s_sub_i32 s19, s3, s0
	s_waitcnt vmcnt(16) lgkmcnt(4)
; #define LAS __attribute__((address_space(3)))
; #define NA_SB() __builtin_amdgcn_sched_barrier(0)
; #define NA_WLOAD(vb_, cw) do { _Pragma("unroll") for (int d = 0; d < 4; ++d) vb_[d] = gld16o(vbase + ((size_t)(d * 16) * SPB + (cw) * 64) * 2, vlo); } while (0)
; #define NA_QK(kb_, s_) do { _Pragma("unroll") for (int t = 0; t < 2; ++t) { f32x4 a = (f32x4){0.f, 0.f, 0.f, 0.f}; a = mfma16(kb_[t][0], q0, a); a = mfma16(kb_[t][1], q1, a); s_[t] = a; } } while (0)
; #define NA_PV(s_, vb_) do { u32x4 pw; pw.x = pk2(s_[0][0], s_[0][1]); pw.y = pk2(s_[0][2], s_[0][3]); pw.z = pk2(s_[1][0], s_[1][1]); pw.w = pk2(s_[1][2], s_[1][3]); const bf16x8 pf = __builtin_bit_cast(bf16x8, pw); \
;         _Pragma("unroll") for (int d = 0; d < 4; ++d) o[d] = mfma16(vb_[d], pf, o[d]); } while (0)
; template <bool WIN>
; __device__ __forceinline__ void na_unit(Frame& F, int b, int h, int r, int strip) {
;     ...
;     bf16x8 vA[4], vB[4], vC[4];
;     if (WIN) { NA_WLOAD(vA, 0); NA_WLOAD(vB, 1); NA_WLOAD(vC, 2); NA_SB(); }
; #pragma unroll
;     for (int cc = 0; cc < 8; ++cc) {
;         bf16x8 kc[2][2], vc[4]; f32x4 sc[2];
; #pragma unroll
;         for (int t = 0; t < 2; ++t) { const LAS bf16_t* kp = KC + (cc * 32 + ki + 4 * t) * 72 + 8 * g; kc[t][0] = *(const LAS bf16x8*)kp; kc[t][1] = *(const LAS bf16x8*)(kp + 32); }
; #pragma unroll
;         for (int d = 0; d < 4; ++d) vc[d] = *(const LAS bf16x8*)(VC + (d * 16 + i) * 264 + cc * 32 + 8 * g);
;         NA_QK(kc, sc);
; #pragma unroll
;         for (int t = 0; t < 2; ++t)
; #pragma unroll
;             for (int e = 0; e < 4; ++e) { const float p = __builtin_amdgcn_exp2f(fminf(sc[t][e], NA_CLAMP)); sc[t][e] = p; lsum += p; }
;         NA_PV(sc, vc);
;     }
	v_mfma_f32_16x16x32_bf16 v[32:35], v[44:47], v[12:15], 0
	v_mfma_f32_16x16x32_bf16 v[36:39], v[52:55], v[12:15], 0
	v_mfma_f32_16x16x32_bf16 v[32:35], v[48:51], v[8:11], v[32:35]
	v_mfma_f32_16x16x32_bf16 v[36:39], v[56:59], v[8:11], v[36:39]
	ds_read_b128 v[44:47], v200 offset:4608
	ds_read_b128 v[48:51], v200 offset:4672
	ds_read_b128 v[52:55], v200 offset:5184
	ds_read_b128 v[56:59], v200 offset:5248
	s_nop 2
	v_min_f32_e32 v32, s18, v32
	v_min_f32_e32 v33, s18, v33
	v_min_f32_e32 v34, s18, v34
	v_min_f32_e32 v35, s18, v35
	v_min_f32_e32 v36, s18, v36
	v_min_f32_e32 v37, s18, v37
	v_min_f32_e32 v38, s18, v38
	v_min_f32_e32 v39, s18, v39
	v_exp_f32_e32 v32, v32
	v_exp_f32_e32 v33, v33
	v_exp_f32_e32 v34, v34
	v_exp_f32_e32 v35, v35
	v_exp_f32_e32 v36, v36
	v_exp_f32_e32 v37, v37
	v_exp_f32_e32 v38, v38
	v_exp_f32_e32 v39, v39
	v_add_f32_e32 v198, v198, v32
	v_add_f32_e32 v199, v199, v36
	v_add_f32_e32 v198, v198, v33
	v_add_f32_e32 v199, v199, v37
	v_add_f32_e32 v198, v198, v34
	v_add_f32_e32 v199, v199, v38
	v_add_f32_e32 v198, v198, v35
	v_add_f32_e32 v199, v199, v39
	v_cvt_pk_bf16_f32 v40, v32, v33
	v_cvt_pk_bf16_f32 v41, v34, v35
	v_cvt_pk_bf16_f32 v42, v36, v37
	v_cvt_pk_bf16_f32 v43, v38, v39
	s_waitcnt lgkmcnt(0)
	v_mfma_f32_16x16x32_bf16 v[32:35], v[44:47], v[12:15], 0
	v_mfma_f32_16x16x32_bf16 v[36:39], v[52:55], v[12:15], 0
	v_mfma_f32_16x16x32_bf16 v[32:35], v[48:51], v[8:11], v[32:35]
	v_mfma_f32_16x16x32_bf16 v[36:39], v[56:59], v[8:11], v[36:39]
	v_mfma_f32_16x16x32_bf16 v[16:19], v[60:63], v[40:43], v[16:19]
	v_mfma_f32_16x16x32_bf16 v[20:23], v[64:67], v[40:43], v[20:23]
	v_mfma_f32_16x16x32_bf16 v[24:27], v[68:71], v[40:43], v[24:27]
	v_mfma_f32_16x16x32_bf16 v[28:31], v[72:75], v[40:43], v[28:31]
	ds_read_b128 v[60:63], v201 offset:64
	ds_read_b128 v[64:67], v201 offset:8512
	ds_read_b128 v[68:71], v201 offset:16960
	ds_read_b128 v[72:75], v201 offset:25408
	ds_read_b128 v[44:47], v200 offset:9216
	ds_read_b128 v[48:51], v200 offset:9280
	ds_read_b128 v[52:55], v200 offset:9792
	ds_read_b128 v[56:59], v200 offset:9856
	v_min_f32_e32 v32, s18, v32
	v_min_f32_e32 v33, s18, v33
	v_min_f32_e32 v34, s18, v34
	v_min_f32_e32 v35, s18, v35
	v_min_f32_e32 v36, s18, v36
	v_min_f32_e32 v37, s18, v37
	v_min_f32_e32 v38, s18, v38
	v_min_f32_e32 v39, s18, v39
	v_exp_f32_e32 v32, v32
	v_exp_f32_e32 v33, v33
	v_exp_f32_e32 v34, v34
	v_exp_f32_e32 v35, v35
	v_exp_f32_e32 v36, v36
	v_exp_f32_e32 v37, v37
	v_exp_f32_e32 v38, v38
	v_exp_f32_e32 v39, v39
	v_add_f32_e32 v198, v198, v32
	v_add_f32_e32 v199, v199, v36
	v_add_f32_e32 v198, v198, v33
	v_add_f32_e32 v199, v199, v37
	v_add_f32_e32 v198, v198, v34
	v_add_f32_e32 v199, v199, v38
	v_add_f32_e32 v198, v198, v35
	v_add_f32_e32 v199, v199, v39
	v_cvt_pk_bf16_f32 v40, v32, v33
	v_cvt_pk_bf16_f32 v41, v34, v35
	v_cvt_pk_bf16_f32 v42, v36, v37
	v_cvt_pk_bf16_f32 v43, v38, v39
	s_waitcnt lgkmcnt(0)
	v_mfma_f32_16x16x32_bf16 v[32:35], v[44:47], v[12:15], 0
	v_mfma_f32_16x16x32_bf16 v[36:39], v[52:55], v[12:15], 0
	v_mfma_f32_16x16x32_bf16 v[32:35], v[48:51], v[8:11], v[32:35]
	v_mfma_f32_16x16x32_bf16 v[36:39], v[56:59], v[8:11], v[36:39]
	v_mfma_f32_16x16x32_bf16 v[16:19], v[60:63], v[40:43], v[16:19]
	v_mfma_f32_16x16x32_bf16 v[20:23], v[64:67], v[40:43], v[20:23]
	v_mfma_f32_16x16x32_bf16 v[24:27], v[68:71], v[40:43], v[24:27]
	v_mfma_f32_16x16x32_bf16 v[28:31], v[72:75], v[40:43], v[28:31]
	ds_read_b128 v[60:63], v201 offset:128
	ds_read_b128 v[64:67], v201 offset:8576
	ds_read_b128 v[68:71], v201 offset:17024
	ds_read_b128 v[72:75], v201 offset:25472
	ds_read_b128 v[44:47], v200 offset:13824
	ds_read_b128 v[48:51], v200 offset:13888
	ds_read_b128 v[52:55], v200 offset:14400
	ds_read_b128 v[56:59], v200 offset:14464
	v_min_f32_e32 v32, s18, v32
	v_min_f32_e32 v33, s18, v33
	v_min_f32_e32 v34, s18, v34
	v_min_f32_e32 v35, s18, v35
	v_min_f32_e32 v36, s18, v36
	v_min_f32_e32 v37, s18, v37
	v_min_f32_e32 v38, s18, v38
	v_min_f32_e32 v39, s18, v39
	v_exp_f32_e32 v32, v32
	v_exp_f32_e32 v33, v33
	v_exp_f32_e32 v34, v34
	v_exp_f32_e32 v35, v35
	v_exp_f32_e32 v36, v36
	v_exp_f32_e32 v37, v37
	v_exp_f32_e32 v38, v38
	v_exp_f32_e32 v39, v39
	v_add_f32_e32 v198, v198, v32
	v_add_f32_e32 v199, v199, v36
	v_add_f32_e32 v198, v198, v33
	v_add_f32_e32 v199, v199, v37
	v_add_f32_e32 v198, v198, v34
	v_add_f32_e32 v199, v199, v38
	v_add_f32_e32 v198, v198, v35
	v_add_f32_e32 v199, v199, v39
	v_cvt_pk_bf16_f32 v40, v32, v33
	v_cvt_pk_bf16_f32 v41, v34, v35
	v_cvt_pk_bf16_f32 v42, v36, v37
	v_cvt_pk_bf16_f32 v43, v38, v39
	s_waitcnt lgkmcnt(0)
	v_mfma_f32_16x16x32_bf16 v[32:35], v[44:47], v[12:15], 0
	v_mfma_f32_16x16x32_bf16 v[36:39], v[52:55], v[12:15], 0
	v_mfma_f32_16x16x32_bf16 v[32:35], v[48:51], v[8:11], v[32:35]
	v_mfma_f32_16x16x32_bf16 v[36:39], v[56:59], v[8:11], v[36:39]
	v_mfma_f32_16x16x32_bf16 v[16:19], v[60:63], v[40:43], v[16:19]
	v_mfma_f32_16x16x32_bf16 v[20:23], v[64:67], v[40:43], v[20:23]
	v_mfma_f32_16x16x32_bf16 v[24:27], v[68:71], v[40:43], v[24:27]
	v_mfma_f32_16x16x32_bf16 v[28:31], v[72:75], v[40:43], v[28:31]
	ds_read_b128 v[60:63], v201 offset:192
	ds_read_b128 v[64:67], v201 offset:8640
	ds_read_b128 v[68:71], v201 offset:17088
	ds_read_b128 v[72:75], v201 offset:25536
	ds_read_b128 v[44:47], v200 offset:18432
	ds_read_b128 v[48:51], v200 offset:18496
	ds_read_b128 v[52:55], v200 offset:19008
	ds_read_b128 v[56:59], v200 offset:19072
	v_min_f32_e32 v32, s18, v32
	v_min_f32_e32 v33, s18, v33
	v_min_f32_e32 v34, s18, v34
	v_min_f32_e32 v35, s18, v35
	v_min_f32_e32 v36, s18, v36
	v_min_f32_e32 v37, s18, v37
	v_min_f32_e32 v38, s18, v38
	v_min_f32_e32 v39, s18, v39
	v_exp_f32_e32 v32, v32
	v_exp_f32_e32 v33, v33
	v_exp_f32_e32 v34, v34
	v_exp_f32_e32 v35, v35
	v_exp_f32_e32 v36, v36
	v_exp_f32_e32 v37, v37
	v_exp_f32_e32 v38, v38
	v_exp_f32_e32 v39, v39
	v_add_f32_e32 v198, v198, v32
	v_add_f32_e32 v199, v199, v36
	v_add_f32_e32 v198, v198, v33
	v_add_f32_e32 v199, v199, v37
	v_add_f32_e32 v198, v198, v34
	v_add_f32_e32 v199, v199, v38
	v_add_f32_e32 v198, v198, v35
	v_add_f32_e32 v199, v199, v39
	v_cvt_pk_bf16_f32 v40, v32, v33
	v_cvt_pk_bf16_f32 v41, v34, v35
	v_cvt_pk_bf16_f32 v42, v36, v37
	v_cvt_pk_bf16_f32 v43, v38, v39
	s_waitcnt lgkmcnt(0)
; #define LAS __attribute__((address_space(3)))
; #define NA_QK(kb_, s_) do { _Pragma("unroll") for (int t = 0; t < 2; ++t) { f32x4 a = (f32x4){0.f, 0.f, 0.f, 0.f}; a = mfma16(kb_[t][0], q0, a); a = mfma16(kb_[t][1], q1, a); s_[t] = a; } } while (0)
; #define NA_PV(s_, vb_) do { u32x4 pw; pw.x = pk2(s_[0][0], s_[0][1]); pw.y = pk2(s_[0][2], s_[0][3]); pw.z = pk2(s_[1][0], s_[1][1]); pw.w = pk2(s_[1][2], s_[1][3]); const bf16x8 pf = __builtin_bit_cast(bf16x8, pw); \
;         _Pragma("unroll") for (int d = 0; d < 4; ++d) o[d] = mfma16(vb_[d], pf, o[d]); } while (0)
; template <bool WIN>
; __device__ __forceinline__ void na_unit(Frame& F, int b, int h, int r, int strip) {
;     ...
; #pragma unroll
;     for (int cc = 0; cc < 8; ++cc) {
;         bf16x8 kc[2][2], vc[4]; f32x4 sc[2];
; #pragma unroll
;         for (int t = 0; t < 2; ++t) { const LAS bf16_t* kp = KC + (cc * 32 + ki + 4 * t) * 72 + 8 * g; kc[t][0] = *(const LAS bf16x8*)kp; kc[t][1] = *(const LAS bf16x8*)(kp + 32); }
; #pragma unroll
;         for (int d = 0; d < 4; ++d) vc[d] = *(const LAS bf16x8*)(VC + (d * 16 + i) * 264 + cc * 32 + 8 * g);
;         NA_QK(kc, sc);
; #pragma unroll
;         for (int t = 0; t < 2; ++t)
; #pragma unroll
;             for (int e = 0; e < 4; ++e) { const float p = __builtin_amdgcn_exp2f(fminf(sc[t][e], NA_CLAMP)); sc[t][e] = p; lsum += p; }
;         NA_PV(sc, vc);
;     }
	v_mfma_f32_16x16x32_bf16 v[32:35], v[44:47], v[12:15], 0
	v_mfma_f32_16x16x32_bf16 v[36:39], v[52:55], v[12:15], 0
	v_mfma_f32_16x16x32_bf16 v[32:35], v[48:51], v[8:11], v[32:35]
	v_mfma_f32_16x16x32_bf16 v[36:39], v[56:59], v[8:11], v[36:39]
	v_mfma_f32_16x16x32_bf16 v[16:19], v[60:63], v[40:43], v[16:19]
	v_mfma_f32_16x16x32_bf16 v[20:23], v[64:67], v[40:43], v[20:23]
	v_mfma_f32_16x16x32_bf16 v[24:27], v[68:71], v[40:43], v[24:27]
	v_mfma_f32_16x16x32_bf16 v[28:31], v[72:75], v[40:43], v[28:31]
	ds_read_b128 v[60:63], v201 offset:256
	ds_read_b128 v[64:67], v201 offset:8704
	ds_read_b128 v[68:71], v201 offset:17152
	ds_read_b128 v[72:75], v201 offset:25600
	ds_read_b128 v[44:47], v200 offset:23040
	ds_read_b128 v[48:51], v200 offset:23104
	ds_read_b128 v[52:55], v200 offset:23616
	ds_read_b128 v[56:59], v200 offset:23680
	v_min_f32_e32 v32, s18, v32
	v_min_f32_e32 v33, s18, v33
	v_min_f32_e32 v34, s18, v34
	v_min_f32_e32 v35, s18, v35
	v_min_f32_e32 v36, s18, v36
	v_min_f32_e32 v37, s18, v37
	v_min_f32_e32 v38, s18, v38
	v_min_f32_e32 v39, s18, v39
	v_exp_f32_e32 v32, v32
	v_exp_f32_e32 v33, v33
	v_exp_f32_e32 v34, v34
	v_exp_f32_e32 v35, v35
	v_exp_f32_e32 v36, v36
	v_exp_f32_e32 v37, v37
	v_exp_f32_e32 v38, v38
	v_exp_f32_e32 v39, v39
	v_add_f32_e32 v198, v198, v32
	v_add_f32_e32 v199, v199, v36
	v_add_f32_e32 v198, v198, v33
	v_add_f32_e32 v199, v199, v37
	v_add_f32_e32 v198, v198, v34
	v_add_f32_e32 v199, v199, v38
	v_add_f32_e32 v198, v198, v35
	v_add_f32_e32 v199, v199, v39
	v_cvt_pk_bf16_f32 v40, v32, v33
	v_cvt_pk_bf16_f32 v41, v34, v35
	v_cvt_pk_bf16_f32 v42, v36, v37
	v_cvt_pk_bf16_f32 v43, v38, v39
	s_waitcnt lgkmcnt(0)
	v_mfma_f32_16x16x32_bf16 v[32:35], v[44:47], v[12:15], 0
	v_mfma_f32_16x16x32_bf16 v[36:39], v[52:55], v[12:15], 0
	v_mfma_f32_16x16x32_bf16 v[32:35], v[48:51], v[8:11], v[32:35]
	v_mfma_f32_16x16x32_bf16 v[36:39], v[56:59], v[8:11], v[36:39]
	v_mfma_f32_16x16x32_bf16 v[16:19], v[60:63], v[40:43], v[16:19]
	v_mfma_f32_16x16x32_bf16 v[20:23], v[64:67], v[40:43], v[20:23]
	v_mfma_f32_16x16x32_bf16 v[24:27], v[68:71], v[40:43], v[24:27]
	v_mfma_f32_16x16x32_bf16 v[28:31], v[72:75], v[40:43], v[28:31]
	ds_read_b128 v[60:63], v201 offset:320
	ds_read_b128 v[64:67], v201 offset:8768
	ds_read_b128 v[68:71], v201 offset:17216
	ds_read_b128 v[72:75], v201 offset:25664
	ds_read_b128 v[44:47], v200 offset:27648
	ds_read_b128 v[48:51], v200 offset:27712
	ds_read_b128 v[52:55], v200 offset:28224
	ds_read_b128 v[56:59], v200 offset:28288
	v_min_f32_e32 v32, s18, v32
	v_min_f32_e32 v33, s18, v33
	v_min_f32_e32 v34, s18, v34
	v_min_f32_e32 v35, s18, v35
	v_min_f32_e32 v36, s18, v36
	v_min_f32_e32 v37, s18, v37
	v_min_f32_e32 v38, s18, v38
	v_min_f32_e32 v39, s18, v39
	v_exp_f32_e32 v32, v32
	v_exp_f32_e32 v33, v33
	v_exp_f32_e32 v34, v34
	v_exp_f32_e32 v35, v35
	v_exp_f32_e32 v36, v36
	v_exp_f32_e32 v37, v37
	v_exp_f32_e32 v38, v38
	v_exp_f32_e32 v39, v39
	v_add_f32_e32 v198, v198, v32
	v_add_f32_e32 v199, v199, v36
	v_add_f32_e32 v198, v198, v33
	v_add_f32_e32 v199, v199, v37
	v_add_f32_e32 v198, v198, v34
	v_add_f32_e32 v199, v199, v38
	v_add_f32_e32 v198, v198, v35
	v_add_f32_e32 v199, v199, v39
	v_cvt_pk_bf16_f32 v40, v32, v33
	v_cvt_pk_bf16_f32 v41, v34, v35
	v_cvt_pk_bf16_f32 v42, v36, v37
	v_cvt_pk_bf16_f32 v43, v38, v39
	s_waitcnt lgkmcnt(0)
	v_mfma_f32_16x16x32_bf16 v[32:35], v[44:47], v[12:15], 0
	v_mfma_f32_16x16x32_bf16 v[36:39], v[52:55], v[12:15], 0
	v_mfma_f32_16x16x32_bf16 v[32:35], v[48:51], v[8:11], v[32:35]
	v_mfma_f32_16x16x32_bf16 v[36:39], v[56:59], v[8:11], v[36:39]
	v_mfma_f32_16x16x32_bf16 v[16:19], v[60:63], v[40:43], v[16:19]
	v_mfma_f32_16x16x32_bf16 v[20:23], v[64:67], v[40:43], v[20:23]
	v_mfma_f32_16x16x32_bf16 v[24:27], v[68:71], v[40:43], v[24:27]
	v_mfma_f32_16x16x32_bf16 v[28:31], v[72:75], v[40:43], v[28:31]
	ds_read_b128 v[60:63], v201 offset:384
	ds_read_b128 v[64:67], v201 offset:8832
	ds_read_b128 v[68:71], v201 offset:17280
	ds_read_b128 v[72:75], v201 offset:25728
	ds_read_b128 v[44:47], v200 offset:32256
	ds_read_b128 v[48:51], v200 offset:32320
	ds_read_b128 v[52:55], v200 offset:32832
	ds_read_b128 v[56:59], v200 offset:32896
	v_min_f32_e32 v32, s18, v32
	v_min_f32_e32 v33, s18, v33
	v_min_f32_e32 v34, s18, v34
	v_min_f32_e32 v35, s18, v35
	v_min_f32_e32 v36, s18, v36
	v_min_f32_e32 v37, s18, v37
	v_min_f32_e32 v38, s18, v38
	v_min_f32_e32 v39, s18, v39
	v_exp_f32_e32 v32, v32
	v_exp_f32_e32 v33, v33
	v_exp_f32_e32 v34, v34
	v_exp_f32_e32 v35, v35
	v_exp_f32_e32 v36, v36
	v_exp_f32_e32 v37, v37
	v_exp_f32_e32 v38, v38
	v_exp_f32_e32 v39, v39
	v_add_f32_e32 v198, v198, v32
	v_add_f32_e32 v199, v199, v36
	v_add_f32_e32 v198, v198, v33
	v_add_f32_e32 v199, v199, v37
	v_add_f32_e32 v198, v198, v34
	v_add_f32_e32 v199, v199, v38
	v_add_f32_e32 v198, v198, v35
	v_add_f32_e32 v199, v199, v39
	v_cvt_pk_bf16_f32 v40, v32, v33
	v_cvt_pk_bf16_f32 v41, v34, v35
	v_cvt_pk_bf16_f32 v42, v36, v37
	v_cvt_pk_bf16_f32 v43, v38, v39
	s_waitcnt lgkmcnt(0)
; #define NA_SB() __builtin_amdgcn_sched_barrier(0)
; #define NA_WLOAD(vb_, cw) do { _Pragma("unroll") for (int d = 0; d < 4; ++d) vb_[d] = gld16o(vbase + ((size_t)(d * 16) * SPB + (cw) * 64) * 2, vlo); } while (0)
; #define NA_PV(s_, vb_) do { u32x4 pw; pw.x = pk2(s_[0][0], s_[0][1]); pw.y = pk2(s_[0][2], s_[0][3]); pw.z = pk2(s_[1][0], s_[1][1]); pw.w = pk2(s_[1][2], s_[1][3]); const bf16x8 pf = __builtin_bit_cast(bf16x8, pw); \
;         _Pragma("unroll") for (int d = 0; d < 4; ++d) o[d] = mfma16(vb_[d], pf, o[d]); } while (0)
; template <bool WIN>
; __device__ __forceinline__ void na_unit(Frame& F, int b, int h, int r, int strip) {
;     ...
;             for (int e = 0; e < 4; ++e) { const float p = __builtin_amdgcn_exp2f(fminf(sc[t][e], NA_CLAMP)); sc[t][e] = p; lsum += p; }
;         NA_PV(sc, vc);
;     }
;     if (WIN) {
;         const int c = strip * 16 + i; int kc0 = c - 8; kc0 = kc0 < 0 ? 0 : (kc0 > 48 ? 48 : kc0);
;         int dcl[2][4]; bool okm[2][4];
; #pragma unroll
;         for (int t = 0; t < 2; ++t)
; #pragma unroll
;             for (int e = 0; e < 4; ++e) { const int kc = u0 + 8 * g + 4 * t + e; okm[t][e] = (kc >= kc0) && (kc < kc0 + 16); int dc = kc - c + 15; dcl[t][e] = okm[t][e] ? (dc < 0 ? 0 : (dc > 30 ? 30 : dc)) : 31; }
;     ...
;         NA_WCHUNK(vA, 0); NA_SB(); NA_WLOAD(vA, 3); NA_SB();
;         NA_WCHUNK(vB, 1); NA_SB(); NA_WLOAD(vB, 4); NA_SB();
;         NA_WCHUNK(vC, 2); NA_SB(); NA_WLOAD(vC, 5); NA_SB();
;         NA_WCHUNK(vA, 3); NA_SB(); NA_WLOAD(vA, 6); NA_SB();
	v_mfma_f32_16x16x32_bf16 v[32:35], v[44:47], v[12:15], 0
	v_mfma_f32_16x16x32_bf16 v[36:39], v[52:55], v[12:15], 0
	v_mfma_f32_16x16x32_bf16 v[32:35], v[48:51], v[8:11], v[32:35]
	v_mfma_f32_16x16x32_bf16 v[36:39], v[56:59], v[8:11], v[36:39]
	v_mfma_f32_16x16x32_bf16 v[16:19], v[60:63], v[40:43], v[16:19]
	v_mfma_f32_16x16x32_bf16 v[20:23], v[64:67], v[40:43], v[20:23]
	v_mfma_f32_16x16x32_bf16 v[24:27], v[68:71], v[40:43], v[24:27]
	v_mfma_f32_16x16x32_bf16 v[28:31], v[72:75], v[40:43], v[28:31]
	ds_read_b128 v[60:63], v201 offset:448
	ds_read_b128 v[64:67], v201 offset:8896
	ds_read_b128 v[68:71], v201 offset:17344
	ds_read_b128 v[72:75], v201 offset:25792
	s_mul_i32 s0, s19, 0x2400
	v_add_u32_e32 v203, s0, v202
	s_add_i32 s19, s19, 1
	s_cmp_eq_u32 s19, 9
	s_cselect_b32 s19, 0, s19
	ds_read_b128 v[44:47], v203 offset:0
	ds_read_b128 v[48:51], v203 offset:64
	ds_read_b128 v[52:55], v203 offset:576
	ds_read_b128 v[56:59], v203 offset:640
	ds_read_b32 v76, v216 offset:0
	ds_read_b32 v77, v217 offset:0
	ds_read_b32 v78, v218 offset:0
	ds_read_b32 v79, v219 offset:0
	ds_read_b32 v80, v220 offset:0
	ds_read_b32 v81, v221 offset:0
	ds_read_b32 v82, v222 offset:0
	ds_read_b32 v83, v223 offset:0
	v_min_f32_e32 v32, s18, v32
	v_min_f32_e32 v33, s18, v33
	v_min_f32_e32 v34, s18, v34
	v_min_f32_e32 v35, s18, v35
	v_min_f32_e32 v36, s18, v36
	v_min_f32_e32 v37, s18, v37
	v_min_f32_e32 v38, s18, v38
	v_min_f32_e32 v39, s18, v39
	v_exp_f32_e32 v32, v32
	v_exp_f32_e32 v33, v33
	v_exp_f32_e32 v34, v34
	v_exp_f32_e32 v35, v35
	v_exp_f32_e32 v36, v36
	v_exp_f32_e32 v37, v37
	v_exp_f32_e32 v38, v38
	v_exp_f32_e32 v39, v39
	v_add_f32_e32 v198, v198, v32
	v_add_f32_e32 v199, v199, v36
	v_add_f32_e32 v198, v198, v33
	v_add_f32_e32 v199, v199, v37
	v_add_f32_e32 v198, v198, v34
	v_add_f32_e32 v199, v199, v38
	v_add_f32_e32 v198, v198, v35
	v_add_f32_e32 v199, v199, v39
	v_cvt_pk_bf16_f32 v40, v32, v33
	v_cvt_pk_bf16_f32 v41, v34, v35
	v_cvt_pk_bf16_f32 v42, v36, v37
	v_cvt_pk_bf16_f32 v43, v38, v39
	s_waitcnt lgkmcnt(8)
	v_mfma_f32_16x16x32_bf16 v[32:35], v[44:47], v[12:15], 0
	v_mfma_f32_16x16x32_bf16 v[36:39], v[52:55], v[12:15], 0
	v_mfma_f32_16x16x32_bf16 v[32:35], v[48:51], v[8:11], v[32:35]
	v_mfma_f32_16x16x32_bf16 v[36:39], v[56:59], v[8:11], v[36:39]
	v_mfma_f32_16x16x32_bf16 v[16:19], v[60:63], v[40:43], v[16:19]
	v_mfma_f32_16x16x32_bf16 v[20:23], v[64:67], v[40:43], v[20:23]
	v_mfma_f32_16x16x32_bf16 v[24:27], v[68:71], v[40:43], v[24:27]
	v_mfma_f32_16x16x32_bf16 v[28:31], v[72:75], v[40:43], v[28:31]
	s_mul_i32 s0, s19, 0x2400
	v_add_u32_e32 v203, s0, v202
	s_add_i32 s19, s19, 1
	s_cmp_eq_u32 s19, 9
	s_cselect_b32 s19, 0, s19
	ds_read_b128 v[44:47], v203 offset:0
	ds_read_b128 v[48:51], v203 offset:64
	ds_read_b128 v[52:55], v203 offset:576
	ds_read_b128 v[56:59], v203 offset:640
	ds_read_b32 v188, v216 offset:128
	ds_read_b32 v189, v217 offset:128
	ds_read_b32 v190, v218 offset:128
	ds_read_b32 v191, v219 offset:128
	ds_read_b32 v194, v220 offset:128
	ds_read_b32 v195, v221 offset:128
	ds_read_b32 v196, v222 offset:128
	ds_read_b32 v197, v223 offset:128
	s_waitcnt lgkmcnt(12)
	v_add_f32_e32 v32, v32, v76
	v_add_f32_e32 v33, v33, v77
	v_add_f32_e32 v34, v34, v78
	v_add_f32_e32 v35, v35, v79
	v_add_f32_e32 v36, v36, v80
	v_add_f32_e32 v37, v37, v81
	v_add_f32_e32 v38, v38, v82
	v_add_f32_e32 v39, v39, v83
	v_min_f32_e32 v32, s18, v32
	v_min_f32_e32 v33, s18, v33
	v_min_f32_e32 v34, s18, v34
	v_min_f32_e32 v35, s18, v35
	v_min_f32_e32 v36, s18, v36
	v_min_f32_e32 v37, s18, v37
	v_min_f32_e32 v38, s18, v38
	v_min_f32_e32 v39, s18, v39
	v_exp_f32_e32 v32, v32
	v_exp_f32_e32 v33, v33
	v_exp_f32_e32 v34, v34
	v_exp_f32_e32 v35, v35
	v_exp_f32_e32 v36, v36
	v_exp_f32_e32 v37, v37
	v_exp_f32_e32 v38, v38
	v_exp_f32_e32 v39, v39
	v_add_f32_e32 v198, v198, v32
	v_add_f32_e32 v199, v199, v36
	v_add_f32_e32 v198, v198, v33
	v_add_f32_e32 v199, v199, v37
	v_add_f32_e32 v198, v198, v34
	v_add_f32_e32 v199, v199, v38
	v_add_f32_e32 v198, v198, v35
	v_add_f32_e32 v199, v199, v39
	v_cvt_pk_bf16_f32 v40, v32, v33
	v_cvt_pk_bf16_f32 v41, v34, v35
	v_cvt_pk_bf16_f32 v42, v36, v37
	v_cvt_pk_bf16_f32 v43, v38, v39
	s_waitcnt lgkmcnt(8)
	v_mfma_f32_16x16x32_bf16 v[32:35], v[44:47], v[12:15], 0
	v_mfma_f32_16x16x32_bf16 v[36:39], v[52:55], v[12:15], 0
	v_mfma_f32_16x16x32_bf16 v[32:35], v[48:51], v[8:11], v[32:35]
	v_mfma_f32_16x16x32_bf16 v[36:39], v[56:59], v[8:11], v[36:39]
	s_waitcnt vmcnt(12)
	v_mfma_f32_16x16x32_bf16 v[16:19], v[104:107], v[40:43], v[16:19]
	v_mfma_f32_16x16x32_bf16 v[20:23], v[108:111], v[40:43], v[20:23]
	v_mfma_f32_16x16x32_bf16 v[24:27], v[112:115], v[40:43], v[24:27]
	v_mfma_f32_16x16x32_bf16 v[28:31], v[116:119], v[40:43], v[28:31]
	global_load_dwordx4 v[104:107], v204, s[20:21] offset:512
	global_load_dwordx4 v[108:111], v205, s[20:21] offset:512
	global_load_dwordx4 v[112:115], v206, s[20:21] offset:512
	global_load_dwordx4 v[116:119], v207, s[20:21] offset:512
	s_mul_i32 s0, s19, 0x2400
	v_add_u32_e32 v203, s0, v202
	s_add_i32 s19, s19, 1
	s_cmp_eq_u32 s19, 9
	s_cselect_b32 s19, 0, s19
	ds_read_b128 v[44:47], v203 offset:0
	ds_read_b128 v[48:51], v203 offset:64
	ds_read_b128 v[52:55], v203 offset:576
	ds_read_b128 v[56:59], v203 offset:640
	ds_read_b32 v76, v216 offset:256
	ds_read_b32 v77, v217 offset:256
	ds_read_b32 v78, v218 offset:256
	ds_read_b32 v79, v219 offset:256
	ds_read_b32 v80, v220 offset:256
	ds_read_b32 v81, v221 offset:256
	ds_read_b32 v82, v222 offset:256
	ds_read_b32 v83, v223 offset:256
	s_waitcnt lgkmcnt(12)
; #define NA_SB() __builtin_amdgcn_sched_barrier(0)
; #define NA_WLOAD(vb_, cw) do { _Pragma("unroll") for (int d = 0; d < 4; ++d) vb_[d] = gld16o(vbase + ((size_t)(d * 16) * SPB + (cw) * 64) * 2, vlo); } while (0)
; template <bool WIN>
; __device__ __forceinline__ void na_unit(Frame& F, int b, int h, int r, int strip) {
;     ...
;         NA_WCHUNK(vA, 0); NA_SB(); NA_WLOAD(vA, 3); NA_SB();
;         NA_WCHUNK(vB, 1); NA_SB(); NA_WLOAD(vB, 4); NA_SB();
;         NA_WCHUNK(vC, 2); NA_SB(); NA_WLOAD(vC, 5); NA_SB();
;         NA_WCHUNK(vA, 3); NA_SB(); NA_WLOAD(vA, 6); NA_SB();
;         NA_WCHUNK(vB, 4); NA_SB(); NA_WLOAD(vB, 7); NA_SB();
	v_add_f32_e32 v32, v32, v188
	v_add_f32_e32 v33, v33, v189
	v_add_f32_e32 v34, v34, v190
	v_add_f32_e32 v35, v35, v191
	v_add_f32_e32 v36, v36, v194
	v_add_f32_e32 v37, v37, v195
	v_add_f32_e32 v38, v38, v196
	v_add_f32_e32 v39, v39, v197
	v_min_f32_e32 v32, s18, v32
	v_min_f32_e32 v33, s18, v33
	v_min_f32_e32 v34, s18, v34
	v_min_f32_e32 v35, s18, v35
	v_min_f32_e32 v36, s18, v36
	v_min_f32_e32 v37, s18, v37
	v_min_f32_e32 v38, s18, v38
	v_min_f32_e32 v39, s18, v39
	v_exp_f32_e32 v32, v32
	v_exp_f32_e32 v33, v33
	v_exp_f32_e32 v34, v34
	v_exp_f32_e32 v35, v35
	v_exp_f32_e32 v36, v36
	v_exp_f32_e32 v37, v37
	v_exp_f32_e32 v38, v38
	v_exp_f32_e32 v39, v39
	v_add_f32_e32 v198, v198, v32
	v_add_f32_e32 v199, v199, v36
	v_add_f32_e32 v198, v198, v33
	v_add_f32_e32 v199, v199, v37
	v_add_f32_e32 v198, v198, v34
	v_add_f32_e32 v199, v199, v38
	v_add_f32_e32 v198, v198, v35
	v_add_f32_e32 v199, v199, v39
	v_cvt_pk_bf16_f32 v40, v32, v33
	v_cvt_pk_bf16_f32 v41, v34, v35
	v_cvt_pk_bf16_f32 v42, v36, v37
	v_cvt_pk_bf16_f32 v43, v38, v39
	s_waitcnt lgkmcnt(8)
	v_mfma_f32_16x16x32_bf16 v[32:35], v[44:47], v[12:15], 0
	v_mfma_f32_16x16x32_bf16 v[36:39], v[52:55], v[12:15], 0
	v_mfma_f32_16x16x32_bf16 v[32:35], v[48:51], v[8:11], v[32:35]
	v_mfma_f32_16x16x32_bf16 v[36:39], v[56:59], v[8:11], v[36:39]
	s_waitcnt vmcnt(12)
	v_mfma_f32_16x16x32_bf16 v[16:19], v[120:123], v[40:43], v[16:19]
	v_mfma_f32_16x16x32_bf16 v[20:23], v[124:127], v[40:43], v[20:23]
	v_mfma_f32_16x16x32_bf16 v[24:27], v[128:131], v[40:43], v[24:27]
	v_mfma_f32_16x16x32_bf16 v[28:31], v[132:135], v[40:43], v[28:31]
	global_load_dwordx4 v[120:123], v204, s[20:21] offset:640
	global_load_dwordx4 v[124:127], v205, s[20:21] offset:640
	global_load_dwordx4 v[128:131], v206, s[20:21] offset:640
	global_load_dwordx4 v[132:135], v207, s[20:21] offset:640
	s_mul_i32 s0, s19, 0x2400
	v_add_u32_e32 v203, s0, v202
	s_add_i32 s19, s19, 1
	s_cmp_eq_u32 s19, 9
	s_cselect_b32 s19, 0, s19
	ds_read_b128 v[44:47], v203 offset:0
	ds_read_b128 v[48:51], v203 offset:64
	ds_read_b128 v[52:55], v203 offset:576
	ds_read_b128 v[56:59], v203 offset:640
	ds_read_b32 v188, v216 offset:384
	ds_read_b32 v189, v217 offset:384
	ds_read_b32 v190, v218 offset:384
	ds_read_b32 v191, v219 offset:384
	ds_read_b32 v194, v220 offset:384
	ds_read_b32 v195, v221 offset:384
	ds_read_b32 v196, v222 offset:384
	ds_read_b32 v197, v223 offset:384
	s_waitcnt lgkmcnt(12)
	v_add_f32_e32 v32, v32, v76
	v_add_f32_e32 v33, v33, v77
	v_add_f32_e32 v34, v34, v78
	v_add_f32_e32 v35, v35, v79
	v_add_f32_e32 v36, v36, v80
	v_add_f32_e32 v37, v37, v81
	v_add_f32_e32 v38, v38, v82
	v_add_f32_e32 v39, v39, v83
	v_min_f32_e32 v32, s18, v32
	v_min_f32_e32 v33, s18, v33
	v_min_f32_e32 v34, s18, v34
	v_min_f32_e32 v35, s18, v35
	v_min_f32_e32 v36, s18, v36
	v_min_f32_e32 v37, s18, v37
	v_min_f32_e32 v38, s18, v38
	v_min_f32_e32 v39, s18, v39
	v_exp_f32_e32 v32, v32
	v_exp_f32_e32 v33, v33
	v_exp_f32_e32 v34, v34
	v_exp_f32_e32 v35, v35
	v_exp_f32_e32 v36, v36
	v_exp_f32_e32 v37, v37
	v_exp_f32_e32 v38, v38
	v_exp_f32_e32 v39, v39
	v_add_f32_e32 v198, v198, v32
	v_add_f32_e32 v199, v199, v36
	v_add_f32_e32 v198, v198, v33
	v_add_f32_e32 v199, v199, v37
	v_add_f32_e32 v198, v198, v34
	v_add_f32_e32 v199, v199, v38
	v_add_f32_e32 v198, v198, v35
	v_add_f32_e32 v199, v199, v39
	v_cvt_pk_bf16_f32 v40, v32, v33
	v_cvt_pk_bf16_f32 v41, v34, v35
	v_cvt_pk_bf16_f32 v42, v36, v37
	v_cvt_pk_bf16_f32 v43, v38, v39
	s_waitcnt lgkmcnt(8)
	v_mfma_f32_16x16x32_bf16 v[32:35], v[44:47], v[12:15], 0
	v_mfma_f32_16x16x32_bf16 v[36:39], v[52:55], v[12:15], 0
	v_mfma_f32_16x16x32_bf16 v[32:35], v[48:51], v[8:11], v[32:35]
	v_mfma_f32_16x16x32_bf16 v[36:39], v[56:59], v[8:11], v[36:39]
	s_waitcnt vmcnt(12)
	v_mfma_f32_16x16x32_bf16 v[16:19], v[156:159], v[40:43], v[16:19]
	v_mfma_f32_16x16x32_bf16 v[20:23], v[160:163], v[40:43], v[20:23]
	v_mfma_f32_16x16x32_bf16 v[24:27], v[164:167], v[40:43], v[24:27]
	v_mfma_f32_16x16x32_bf16 v[28:31], v[168:171], v[40:43], v[28:31]
	global_load_dwordx4 v[156:159], v204, s[20:21] offset:768
	global_load_dwordx4 v[160:163], v205, s[20:21] offset:768
	global_load_dwordx4 v[164:167], v206, s[20:21] offset:768
	global_load_dwordx4 v[168:171], v207, s[20:21] offset:768
	s_mul_i32 s0, s19, 0x2400
	v_add_u32_e32 v203, s0, v202
	s_add_i32 s19, s19, 1
	s_cmp_eq_u32 s19, 9
	s_cselect_b32 s19, 0, s19
	ds_read_b128 v[44:47], v203 offset:0
	ds_read_b128 v[48:51], v203 offset:64
	ds_read_b128 v[52:55], v203 offset:576
	ds_read_b128 v[56:59], v203 offset:640
	ds_read_b32 v76, v216 offset:512
	ds_read_b32 v77, v217 offset:512
	ds_read_b32 v78, v218 offset:512
	ds_read_b32 v79, v219 offset:512
	ds_read_b32 v80, v220 offset:512
	ds_read_b32 v81, v221 offset:512
	ds_read_b32 v82, v222 offset:512
	ds_read_b32 v83, v223 offset:512
	s_waitcnt lgkmcnt(12)
	v_add_f32_e32 v32, v32, v188
	v_add_f32_e32 v33, v33, v189
	v_add_f32_e32 v34, v34, v190
	v_add_f32_e32 v35, v35, v191
	v_add_f32_e32 v36, v36, v194
	v_add_f32_e32 v37, v37, v195
	v_add_f32_e32 v38, v38, v196
	v_add_f32_e32 v39, v39, v197
	v_min_f32_e32 v32, s18, v32
	v_min_f32_e32 v33, s18, v33
	v_min_f32_e32 v34, s18, v34
	v_min_f32_e32 v35, s18, v35
	v_min_f32_e32 v36, s18, v36
	v_min_f32_e32 v37, s18, v37
	v_min_f32_e32 v38, s18, v38
	v_min_f32_e32 v39, s18, v39
	v_exp_f32_e32 v32, v32
	v_exp_f32_e32 v33, v33
	v_exp_f32_e32 v34, v34
	v_exp_f32_e32 v35, v35
	v_exp_f32_e32 v36, v36
	v_exp_f32_e32 v37, v37
	v_exp_f32_e32 v38, v38
	v_exp_f32_e32 v39, v39
	v_add_f32_e32 v198, v198, v32
	v_add_f32_e32 v199, v199, v36
	v_add_f32_e32 v198, v198, v33
	v_add_f32_e32 v199, v199, v37
	v_add_f32_e32 v198, v198, v34
	v_add_f32_e32 v199, v199, v38
	v_add_f32_e32 v198, v198, v35
	v_add_f32_e32 v199, v199, v39
	v_cvt_pk_bf16_f32 v40, v32, v33
	v_cvt_pk_bf16_f32 v41, v34, v35
	v_cvt_pk_bf16_f32 v42, v36, v37
	v_cvt_pk_bf16_f32 v43, v38, v39
	s_waitcnt lgkmcnt(8)
; #define NA_SB() __builtin_amdgcn_sched_barrier(0)
; #define NA_WLOAD(vb_, cw) do { _Pragma("unroll") for (int d = 0; d < 4; ++d) vb_[d] = gld16o(vbase + ((size_t)(d * 16) * SPB + (cw) * 64) * 2, vlo); } while (0)
; template <bool WIN>
; __device__ __forceinline__ void na_unit(Frame& F, int b, int h, int r, int strip) {
;     ...
;         NA_WCHUNK(vA, 0); NA_SB(); NA_WLOAD(vA, 3); NA_SB();
;         NA_WCHUNK(vB, 1); NA_SB(); NA_WLOAD(vB, 4); NA_SB();
;         NA_WCHUNK(vC, 2); NA_SB(); NA_WLOAD(vC, 5); NA_SB();
;         NA_WCHUNK(vA, 3); NA_SB(); NA_WLOAD(vA, 6); NA_SB();
;         NA_WCHUNK(vB, 4); NA_SB(); NA_WLOAD(vB, 7); NA_SB();
;         NA_WCHUNK(vC, 5); NA_SB();
;         NA_WCHUNK(vA, 6); NA_SB();
	v_mfma_f32_16x16x32_bf16 v[32:35], v[44:47], v[12:15], 0
	v_mfma_f32_16x16x32_bf16 v[36:39], v[52:55], v[12:15], 0
	v_mfma_f32_16x16x32_bf16 v[32:35], v[48:51], v[8:11], v[32:35]
	v_mfma_f32_16x16x32_bf16 v[36:39], v[56:59], v[8:11], v[36:39]
	s_waitcnt vmcnt(12)
	v_mfma_f32_16x16x32_bf16 v[16:19], v[172:175], v[40:43], v[16:19]
	v_mfma_f32_16x16x32_bf16 v[20:23], v[176:179], v[40:43], v[20:23]
	v_mfma_f32_16x16x32_bf16 v[24:27], v[180:183], v[40:43], v[24:27]
	v_mfma_f32_16x16x32_bf16 v[28:31], v[184:187], v[40:43], v[28:31]
	global_load_dwordx4 v[172:175], v204, s[20:21] offset:896
	global_load_dwordx4 v[176:179], v205, s[20:21] offset:896
	global_load_dwordx4 v[180:183], v206, s[20:21] offset:896
	global_load_dwordx4 v[184:187], v207, s[20:21] offset:896
	s_mul_i32 s0, s19, 0x2400
	v_add_u32_e32 v203, s0, v202
	s_add_i32 s19, s19, 1
	s_cmp_eq_u32 s19, 9
	s_cselect_b32 s19, 0, s19
	ds_read_b128 v[44:47], v203 offset:0
	ds_read_b128 v[48:51], v203 offset:64
	ds_read_b128 v[52:55], v203 offset:576
	ds_read_b128 v[56:59], v203 offset:640
	ds_read_b32 v188, v216 offset:640
	ds_read_b32 v189, v217 offset:640
	ds_read_b32 v190, v218 offset:640
	ds_read_b32 v191, v219 offset:640
	ds_read_b32 v194, v220 offset:640
	ds_read_b32 v195, v221 offset:640
	ds_read_b32 v196, v222 offset:640
	ds_read_b32 v197, v223 offset:640
	s_waitcnt lgkmcnt(12)
	v_add_f32_e32 v32, v32, v76
	v_add_f32_e32 v33, v33, v77
	v_add_f32_e32 v34, v34, v78
	v_add_f32_e32 v35, v35, v79
	v_add_f32_e32 v36, v36, v80
	v_add_f32_e32 v37, v37, v81
	v_add_f32_e32 v38, v38, v82
	v_add_f32_e32 v39, v39, v83
	v_min_f32_e32 v32, s18, v32
	v_min_f32_e32 v33, s18, v33
	v_min_f32_e32 v34, s18, v34
	v_min_f32_e32 v35, s18, v35
	v_min_f32_e32 v36, s18, v36
	v_min_f32_e32 v37, s18, v37
	v_min_f32_e32 v38, s18, v38
	v_min_f32_e32 v39, s18, v39
	v_exp_f32_e32 v32, v32
	v_exp_f32_e32 v33, v33
	v_exp_f32_e32 v34, v34
	v_exp_f32_e32 v35, v35
	v_exp_f32_e32 v36, v36
	v_exp_f32_e32 v37, v37
	v_exp_f32_e32 v38, v38
	v_exp_f32_e32 v39, v39
	v_add_f32_e32 v198, v198, v32
	v_add_f32_e32 v199, v199, v36
	v_add_f32_e32 v198, v198, v33
	v_add_f32_e32 v199, v199, v37
	v_add_f32_e32 v198, v198, v34
	v_add_f32_e32 v199, v199, v38
	v_add_f32_e32 v198, v198, v35
	v_add_f32_e32 v199, v199, v39
	v_cvt_pk_bf16_f32 v40, v32, v33
	v_cvt_pk_bf16_f32 v41, v34, v35
	v_cvt_pk_bf16_f32 v42, v36, v37
	v_cvt_pk_bf16_f32 v43, v38, v39
	s_waitcnt lgkmcnt(8)
	v_mfma_f32_16x16x32_bf16 v[32:35], v[44:47], v[12:15], 0
	v_mfma_f32_16x16x32_bf16 v[36:39], v[52:55], v[12:15], 0
	v_mfma_f32_16x16x32_bf16 v[32:35], v[48:51], v[8:11], v[32:35]
	v_mfma_f32_16x16x32_bf16 v[36:39], v[56:59], v[8:11], v[36:39]
	s_waitcnt vmcnt(12)
	v_mfma_f32_16x16x32_bf16 v[16:19], v[104:107], v[40:43], v[16:19]
	v_mfma_f32_16x16x32_bf16 v[20:23], v[108:111], v[40:43], v[20:23]
	v_mfma_f32_16x16x32_bf16 v[24:27], v[112:115], v[40:43], v[24:27]
	v_mfma_f32_16x16x32_bf16 v[28:31], v[116:119], v[40:43], v[28:31]
	s_mul_i32 s0, s19, 0x2400
	v_add_u32_e32 v203, s0, v202
	s_add_i32 s19, s19, 1
	s_cmp_eq_u32 s19, 9
	s_cselect_b32 s19, 0, s19
	ds_read_b128 v[44:47], v203 offset:0
	ds_read_b128 v[48:51], v203 offset:64
	ds_read_b128 v[52:55], v203 offset:576
	ds_read_b128 v[56:59], v203 offset:640
	ds_read_b32 v76, v216 offset:768
	ds_read_b32 v77, v217 offset:768
	ds_read_b32 v78, v218 offset:768
	ds_read_b32 v79, v219 offset:768
	ds_read_b32 v80, v220 offset:768
	ds_read_b32 v81, v221 offset:768
	ds_read_b32 v82, v222 offset:768
	ds_read_b32 v83, v223 offset:768
	s_waitcnt lgkmcnt(12)
	v_add_f32_e32 v32, v32, v188
	v_add_f32_e32 v33, v33, v189
	v_add_f32_e32 v34, v34, v190
	v_add_f32_e32 v35, v35, v191
	v_add_f32_e32 v36, v36, v194
	v_add_f32_e32 v37, v37, v195
	v_add_f32_e32 v38, v38, v196
	v_add_f32_e32 v39, v39, v197
	v_min_f32_e32 v32, s18, v32
	v_min_f32_e32 v33, s18, v33
	v_min_f32_e32 v34, s18, v34
	v_min_f32_e32 v35, s18, v35
	v_min_f32_e32 v36, s18, v36
	v_min_f32_e32 v37, s18, v37
	v_min_f32_e32 v38, s18, v38
	v_min_f32_e32 v39, s18, v39
	v_exp_f32_e32 v32, v32
	v_exp_f32_e32 v33, v33
	v_exp_f32_e32 v34, v34
	v_exp_f32_e32 v35, v35
	v_exp_f32_e32 v36, v36
	v_exp_f32_e32 v37, v37
	v_exp_f32_e32 v38, v38
	v_exp_f32_e32 v39, v39
	v_add_f32_e32 v198, v198, v32
	v_add_f32_e32 v199, v199, v36
	v_add_f32_e32 v198, v198, v33
	v_add_f32_e32 v199, v199, v37
	v_add_f32_e32 v198, v198, v34
	v_add_f32_e32 v199, v199, v38
	v_add_f32_e32 v198, v198, v35
	v_add_f32_e32 v199, v199, v39
	v_cvt_pk_bf16_f32 v40, v32, v33
	v_cvt_pk_bf16_f32 v41, v34, v35
	v_cvt_pk_bf16_f32 v42, v36, v37
	v_cvt_pk_bf16_f32 v43, v38, v39
	s_waitcnt lgkmcnt(8)
	v_mfma_f32_16x16x32_bf16 v[32:35], v[44:47], v[12:15], 0
	v_mfma_f32_16x16x32_bf16 v[36:39], v[52:55], v[12:15], 0
	v_mfma_f32_16x16x32_bf16 v[32:35], v[48:51], v[8:11], v[32:35]
	v_mfma_f32_16x16x32_bf16 v[36:39], v[56:59], v[8:11], v[36:39]
	s_waitcnt vmcnt(8)
; #define GAS __attribute__((address_space(1)))
; __device__ __forceinline__ unsigned pk2(float lo, float hi) { const f32x2 v = {lo, hi}; const bf16v2 b = __builtin_convertvector(v, bf16v2); return __builtin_bit_cast(unsigned, b); }
; __device__ __forceinline__ float shx(float v, int o, int lane) { return __builtin_bit_cast(float, __builtin_amdgcn_ds_bpermute((lane ^ o) << 2, __builtin_bit_cast(int, v))); }
; __device__ __forceinline__ const char* uni_ptr(const char* p) { const unsigned long long v = (unsigned long long)p; const unsigned lo = __builtin_amdgcn_readfirstlane((unsigned)v), hi = __builtin_amdgcn_readfirstlane((unsigned)(v >> 32)); return (const char*)(((unsigned long long)hi << 32) | lo); }
; #define NA_SB() __builtin_amdgcn_sched_barrier(0)
; #define NA_WLOAD(vb_, cw) do { _Pragma("unroll") for (int d = 0; d < 4; ++d) vb_[d] = gld16o(vbase + ((size_t)(d * 16) * SPB + (cw) * 64) * 2, vlo); } while (0)
; template <bool WIN>
; __device__ __forceinline__ void na_unit(Frame& F, int b, int h, int r, int strip) {
;     ...
;         NA_WCHUNK(vC, 2); NA_SB(); NA_WLOAD(vC, 5); NA_SB();
;         NA_WCHUNK(vA, 3); NA_SB(); NA_WLOAD(vA, 6); NA_SB();
;         NA_WCHUNK(vB, 4); NA_SB(); NA_WLOAD(vB, 7); NA_SB();
;         NA_WCHUNK(vC, 5); NA_SB();
;         NA_WCHUNK(vA, 6); NA_SB();
;         NA_WCHUNK(vB, 7); NA_SB();
;     ...
;     }
;     lsum += shx(lsum, 16, ln_); lsum += shx(lsum, 32, ln_);
;     const float inv = 1.0f / lsum;
;     char* op = (char*)uni_ptr((const char*)((bf16_t*)(F.ws + WS_MIX) + (size_t)qrow0 * DM + h * 64)); const unsigned olo = (unsigned)((i * DM + 4 * g) * 2);
; #pragma unroll
;     for (int d = 0; d < 4; ++d) { u32x2 w; w.x = pk2(o[d][0] * inv, o[d][1] * inv); w.y = pk2(o[d][2] * inv, o[d][3] * inv); *(GAS u32x2*)(op + d * 32 + (size_t)olo) = w; }
	v_mfma_f32_16x16x32_bf16 v[16:19], v[120:123], v[40:43], v[16:19]
	v_mfma_f32_16x16x32_bf16 v[20:23], v[124:127], v[40:43], v[20:23]
	v_mfma_f32_16x16x32_bf16 v[24:27], v[128:131], v[40:43], v[24:27]
	v_mfma_f32_16x16x32_bf16 v[28:31], v[132:135], v[40:43], v[28:31]
	s_mul_i32 s0, s19, 0x2400
	v_add_u32_e32 v203, s0, v202
	s_add_i32 s19, s19, 1
	s_cmp_eq_u32 s19, 9
	s_cselect_b32 s19, 0, s19
	ds_read_b128 v[44:47], v203 offset:0
	ds_read_b128 v[48:51], v203 offset:64
	ds_read_b128 v[52:55], v203 offset:576
	ds_read_b128 v[56:59], v203 offset:640
	ds_read_b32 v188, v216 offset:896
	ds_read_b32 v189, v217 offset:896
	ds_read_b32 v190, v218 offset:896
	ds_read_b32 v191, v219 offset:896
	ds_read_b32 v194, v220 offset:896
	ds_read_b32 v195, v221 offset:896
	ds_read_b32 v196, v222 offset:896
	ds_read_b32 v197, v223 offset:896
	s_waitcnt lgkmcnt(12)
	v_add_f32_e32 v32, v32, v76
	v_add_f32_e32 v33, v33, v77
	v_add_f32_e32 v34, v34, v78
	v_add_f32_e32 v35, v35, v79
	v_add_f32_e32 v36, v36, v80
	v_add_f32_e32 v37, v37, v81
	v_add_f32_e32 v38, v38, v82
	v_add_f32_e32 v39, v39, v83
	v_min_f32_e32 v32, s18, v32
	v_min_f32_e32 v33, s18, v33
	v_min_f32_e32 v34, s18, v34
	v_min_f32_e32 v35, s18, v35
	v_min_f32_e32 v36, s18, v36
	v_min_f32_e32 v37, s18, v37
	v_min_f32_e32 v38, s18, v38
	v_min_f32_e32 v39, s18, v39
	v_exp_f32_e32 v32, v32
	v_exp_f32_e32 v33, v33
	v_exp_f32_e32 v34, v34
	v_exp_f32_e32 v35, v35
	v_exp_f32_e32 v36, v36
	v_exp_f32_e32 v37, v37
	v_exp_f32_e32 v38, v38
	v_exp_f32_e32 v39, v39
	v_add_f32_e32 v198, v198, v32
	v_add_f32_e32 v199, v199, v36
	v_add_f32_e32 v198, v198, v33
	v_add_f32_e32 v199, v199, v37
	v_add_f32_e32 v198, v198, v34
	v_add_f32_e32 v199, v199, v38
	v_add_f32_e32 v198, v198, v35
	v_add_f32_e32 v199, v199, v39
	v_cvt_pk_bf16_f32 v40, v32, v33
	v_cvt_pk_bf16_f32 v41, v34, v35
	v_cvt_pk_bf16_f32 v42, v36, v37
	v_cvt_pk_bf16_f32 v43, v38, v39
	s_waitcnt lgkmcnt(8)
	v_mfma_f32_16x16x32_bf16 v[32:35], v[44:47], v[12:15], 0
	v_mfma_f32_16x16x32_bf16 v[36:39], v[52:55], v[12:15], 0
	v_mfma_f32_16x16x32_bf16 v[32:35], v[48:51], v[8:11], v[32:35]
	v_mfma_f32_16x16x32_bf16 v[36:39], v[56:59], v[8:11], v[36:39]
	s_waitcnt vmcnt(4)
	v_mfma_f32_16x16x32_bf16 v[16:19], v[156:159], v[40:43], v[16:19]
	v_mfma_f32_16x16x32_bf16 v[20:23], v[160:163], v[40:43], v[20:23]
	v_mfma_f32_16x16x32_bf16 v[24:27], v[164:167], v[40:43], v[24:27]
	v_mfma_f32_16x16x32_bf16 v[28:31], v[168:171], v[40:43], v[28:31]
	s_waitcnt lgkmcnt(0)
	s_nop 0
	v_add_f32_e32 v32, v32, v188
	v_add_f32_e32 v33, v33, v189
	v_add_f32_e32 v34, v34, v190
	v_add_f32_e32 v35, v35, v191
	v_add_f32_e32 v36, v36, v194
	v_add_f32_e32 v37, v37, v195
	v_add_f32_e32 v38, v38, v196
	v_add_f32_e32 v39, v39, v197
	v_min_f32_e32 v32, s18, v32
	v_min_f32_e32 v33, s18, v33
	v_min_f32_e32 v34, s18, v34
	v_min_f32_e32 v35, s18, v35
	v_min_f32_e32 v36, s18, v36
	v_min_f32_e32 v37, s18, v37
	v_min_f32_e32 v38, s18, v38
	v_min_f32_e32 v39, s18, v39
	v_exp_f32_e32 v32, v32
	v_exp_f32_e32 v33, v33
	v_exp_f32_e32 v34, v34
	v_exp_f32_e32 v35, v35
	v_exp_f32_e32 v36, v36
	v_exp_f32_e32 v37, v37
	v_exp_f32_e32 v38, v38
	v_exp_f32_e32 v39, v39
	v_add_f32_e32 v198, v198, v32
	v_add_f32_e32 v199, v199, v36
	v_add_f32_e32 v198, v198, v33
	v_add_f32_e32 v199, v199, v37
	v_add_f32_e32 v198, v198, v34
	v_add_f32_e32 v199, v199, v38
	v_add_f32_e32 v198, v198, v35
	v_add_f32_e32 v199, v199, v39
	v_cvt_pk_bf16_f32 v40, v32, v33
	v_cvt_pk_bf16_f32 v41, v34, v35
	v_cvt_pk_bf16_f32 v42, v36, v37
	v_cvt_pk_bf16_f32 v43, v38, v39
	s_waitcnt vmcnt(0)
	s_nop 0
	v_mfma_f32_16x16x32_bf16 v[16:19], v[172:175], v[40:43], v[16:19]
	v_mfma_f32_16x16x32_bf16 v[20:23], v[176:179], v[40:43], v[20:23]
	v_mfma_f32_16x16x32_bf16 v[24:27], v[180:183], v[40:43], v[24:27]
	v_mfma_f32_16x16x32_bf16 v[28:31], v[184:187], v[40:43], v[28:31]
	v_add_f32_e32 v198, v198, v199
	ds_bpermute_b32 v237, v246, v198
	s_waitcnt lgkmcnt(0)
	v_add_f32_e32 v198, v198, v237
	ds_bpermute_b32 v237, v247, v198
	s_waitcnt lgkmcnt(0)
	v_add_f32_e32 v198, v198, v237
	v_rcp_f32_e32 v225, v198
	s_nop 0
	v_fma_f32 v236, -v198, v225, 1.0
	v_fma_f32 v225, v236, v225, v225
	v_mul_f32_e32 v16, v16, v225
	v_mul_f32_e32 v17, v17, v225
	v_mul_f32_e32 v18, v18, v225
	v_mul_f32_e32 v19, v19, v225
	v_mul_f32_e32 v20, v20, v225
	v_mul_f32_e32 v21, v21, v225
	v_mul_f32_e32 v22, v22, v225
	v_mul_f32_e32 v23, v23, v225
	v_mul_f32_e32 v24, v24, v225
	v_mul_f32_e32 v25, v25, v225
	v_mul_f32_e32 v26, v26, v225
	v_mul_f32_e32 v27, v27, v225
	v_mul_f32_e32 v28, v28, v225
	v_mul_f32_e32 v29, v29, v225
	v_mul_f32_e32 v30, v30, v225
	v_mul_f32_e32 v31, v31, v225
	v_cvt_pk_bf16_f32 v16, v16, v17
	v_cvt_pk_bf16_f32 v17, v18, v19
	v_cvt_pk_bf16_f32 v20, v20, v21
	v_cvt_pk_bf16_f32 v21, v22, v23
	v_cvt_pk_bf16_f32 v24, v24, v25
	v_cvt_pk_bf16_f32 v25, v26, v27
	v_cvt_pk_bf16_f32 v28, v28, v29
	v_cvt_pk_bf16_f32 v29, v30, v31
	global_store_dwordx2 v224, v[16:17], s[10:11] offset:0
	global_store_dwordx2 v224, v[20:21], s[10:11] offset:32
	global_store_dwordx2 v224, v[24:25], s[10:11] offset:64
	global_store_dwordx2 v224, v[28:29], s[10:11] offset:96
	s_andn2_b64 vcc, exec, s[50:51]
	s_barrier
	s_cbranch_vccnz .LBB0_495
	s_mul_hi_u32 s0, s84, 0x38e38e39
	s_lshr_b32 s0, s0, 1
	s_mul_i32 s0, s0, 9
	s_sub_i32 s0, s84, s0
	s_mulk_i32 s0, 0x2400
	v_add_u32_e32 v8, s0, v97
	ds_write_b128 v8, v[0:3]

; #define GAS __attribute__((address_space(1)))
;     __device__ __forceinline__ void operator()(const f32x4 (&acc)[2][2][4][2], const Unit& u, int wr, int wc, int fr, int fq, const Pre& pre, bool drain) const {
;     ...
;             u32x2 o[2][4];
; #pragma unroll
;             for (int ai = 0; ai < 2; ++ai)
; #pragma unroll
;                 for (int m = 0; m < 4; ++m) { unsigned w[2];
; #pragma unroll
;                     for (int bj = 0; bj < 2; ++bj) { const f32x4 v0 = acc[ai][bj][m][0], v1 = acc[ai][bj][m][1];
;                         unsigned x = 0u;
;                         x = __builtin_amdgcn_cvt_scalef32_pk_fp4_f32(x, v0[0], v0[1], 1.0f, 0); x = __builtin_amdgcn_cvt_scalef32_pk_fp4_f32(x, v0[2], v0[3], 1.0f, 1);
;                         x = __builtin_amdgcn_cvt_scalef32_pk_fp4_f32(x, v1[0], v1[1], 1.0f, 2); x = __builtin_amdgcn_cvt_scalef32_pk_fp4_f32(x, v1[2], v1[3], 1.0f, 3);
;                         w[bj] = x; }
;                     o[ai][m] = (u32x2){w[0], w[1]}; }
;             if (drain) asm volatile("s_waitcnt vmcnt(0)" ::: "memory");
; #pragma unroll
;             for (int ai = 0; ai < 2; ++ai)
; #pragma unroll
;                 for (int m = 0; m < 4; ++m) { const int dst = pre.tab[wr * 64 + fr + ai * HALF + m * 16];
;                     if (dst >= 0) *(GAS u32x2*)(Y2 + (size_t)dst * 512 + (u.ocol0 >> 1) + wc * 32 + fq * 8) = o[ai][m]; }
.LBB0_1543:
	s_or_b64 exec, exec, s[2:3]
	s_add_i32 s0, s76, 0
	v_lshl_add_u32 v139, v164, 2, s0
	v_add_u32_e32 v139, 0x20000, v139
	s_lshl_b32 s2, s18, 7
	s_ashr_i32 s3, s2, 31
	ds_read_b32 v172, v139
	ds_read_b32 v173, v139 offset:64
	ds_read_b32 v174, v139 offset:128
	ds_read_b32 v175, v139 offset:192
	ds_read_b32 v176, v139 offset:512
	ds_read_b32 v177, v139 offset:576
	ds_read_b32 v178, v139 offset:640
	ds_read_b32 v179, v139 offset:704
	s_add_i32 s0, s2, s22
	v_add_u32_e32 v180, s0, v142
	v_cvt_scalef32_pk_fp4_f32 v182, v112, v113, 1.0
	v_cvt_scalef32_pk_fp4_f32 v183, v120, v121, 1.0
	v_cvt_scalef32_pk_fp4_f32 v182, v114, v115, 1.0 op_sel:[0,0,1,0]
	v_cvt_scalef32_pk_fp4_f32 v183, v122, v123, 1.0 op_sel:[0,0,1,0]
	v_cvt_scalef32_pk_fp4_f32 v182, v116, v117, 1.0 op_sel:[0,0,0,1]
	v_cvt_scalef32_pk_fp4_f32 v183, v124, v125, 1.0 op_sel:[0,0,0,1]
	v_cvt_scalef32_pk_fp4_f32 v182, v118, v119, 1.0 op_sel:[0,0,1,1]
	v_cvt_scalef32_pk_fp4_f32 v183, v126, v127, 1.0 op_sel:[0,0,1,1]
	s_waitcnt lgkmcnt(7)
	v_cmp_lt_i32_e32 vcc, -1, v172
	v_lshl_add_u32 v181, v172, 9, v180
	s_and_saveexec_b64 s[50:51], vcc
	global_store_dwordx2 v181, v[182:183], s[48:49]
	s_or_b64 exec, exec, s[50:51]
	v_cvt_scalef32_pk_fp4_f32 v184, v96, v97, 1.0
	v_cvt_scalef32_pk_fp4_f32 v185, v104, v105, 1.0
	v_cvt_scalef32_pk_fp4_f32 v184, v98, v99, 1.0 op_sel:[0,0,1,0]
	v_cvt_scalef32_pk_fp4_f32 v185, v106, v107, 1.0 op_sel:[0,0,1,0]
	v_cvt_scalef32_pk_fp4_f32 v184, v100, v101, 1.0 op_sel:[0,0,0,1]
	v_cvt_scalef32_pk_fp4_f32 v185, v108, v109, 1.0 op_sel:[0,0,0,1]
	v_cvt_scalef32_pk_fp4_f32 v184, v102, v103, 1.0 op_sel:[0,0,1,1]
	v_cvt_scalef32_pk_fp4_f32 v185, v110, v111, 1.0 op_sel:[0,0,1,1]
	s_waitcnt lgkmcnt(6)
	v_cmp_lt_i32_e32 vcc, -1, v173
	v_lshl_add_u32 v181, v173, 9, v180
	s_and_saveexec_b64 s[50:51], vcc
	global_store_dwordx2 v181, v[184:185], s[48:49]
	s_or_b64 exec, exec, s[50:51]
	v_cvt_scalef32_pk_fp4_f32 v182, v64, v65, 1.0
	v_cvt_scalef32_pk_fp4_f32 v183, v80, v81, 1.0
	v_cvt_scalef32_pk_fp4_f32 v182, v66, v67, 1.0 op_sel:[0,0,1,0]
	v_cvt_scalef32_pk_fp4_f32 v183, v82, v83, 1.0 op_sel:[0,0,1,0]
	v_cvt_scalef32_pk_fp4_f32 v182, v68, v69, 1.0 op_sel:[0,0,0,1]
	v_cvt_scalef32_pk_fp4_f32 v183, v84, v85, 1.0 op_sel:[0,0,0,1]
	v_cvt_scalef32_pk_fp4_f32 v182, v70, v71, 1.0 op_sel:[0,0,1,1]
	v_cvt_scalef32_pk_fp4_f32 v183, v86, v87, 1.0 op_sel:[0,0,1,1]
	s_waitcnt lgkmcnt(5)
	v_cmp_lt_i32_e32 vcc, -1, v174
	v_lshl_add_u32 v181, v174, 9, v180
	s_and_saveexec_b64 s[50:51], vcc
	global_store_dwordx2 v181, v[182:183], s[48:49]
	s_or_b64 exec, exec, s[50:51]
	v_cvt_scalef32_pk_fp4_f32 v184, v32, v33, 1.0
	v_cvt_scalef32_pk_fp4_f32 v185, v48, v49, 1.0
	v_cvt_scalef32_pk_fp4_f32 v184, v34, v35, 1.0 op_sel:[0,0,1,0]
	v_cvt_scalef32_pk_fp4_f32 v185, v50, v51, 1.0 op_sel:[0,0,1,0]
	v_cvt_scalef32_pk_fp4_f32 v184, v36, v37, 1.0 op_sel:[0,0,0,1]
	v_cvt_scalef32_pk_fp4_f32 v185, v52, v53, 1.0 op_sel:[0,0,0,1]
	v_cvt_scalef32_pk_fp4_f32 v184, v38, v39, 1.0 op_sel:[0,0,1,1]
	v_cvt_scalef32_pk_fp4_f32 v185, v54, v55, 1.0 op_sel:[0,0,1,1]
	s_waitcnt lgkmcnt(4)
	v_cmp_lt_i32_e32 vcc, -1, v175
	v_lshl_add_u32 v181, v175, 9, v180
	s_and_saveexec_b64 s[50:51], vcc
	global_store_dwordx2 v181, v[184:185], s[48:49]
	s_or_b64 exec, exec, s[50:51]
	v_cvt_scalef32_pk_fp4_f32 v182, v72, v73, 1.0
	v_cvt_scalef32_pk_fp4_f32 v183, v88, v89, 1.0
	v_cvt_scalef32_pk_fp4_f32 v182, v74, v75, 1.0 op_sel:[0,0,1,0]
	v_cvt_scalef32_pk_fp4_f32 v183, v90, v91, 1.0 op_sel:[0,0,1,0]
	v_cvt_scalef32_pk_fp4_f32 v182, v76, v77, 1.0 op_sel:[0,0,0,1]
	v_cvt_scalef32_pk_fp4_f32 v183, v92, v93, 1.0 op_sel:[0,0,0,1]
	v_cvt_scalef32_pk_fp4_f32 v182, v78, v79, 1.0 op_sel:[0,0,1,1]
	v_cvt_scalef32_pk_fp4_f32 v183, v94, v95, 1.0 op_sel:[0,0,1,1]
	s_waitcnt lgkmcnt(3)
	v_cmp_lt_i32_e32 vcc, -1, v176
	v_lshl_add_u32 v181, v176, 9, v180
	s_and_saveexec_b64 s[50:51], vcc
	global_store_dwordx2 v181, v[182:183], s[48:49]
	s_or_b64 exec, exec, s[50:51]
	v_cvt_scalef32_pk_fp4_f32 v184, v40, v41, 1.0
	v_cvt_scalef32_pk_fp4_f32 v185, v56, v57, 1.0
	v_cvt_scalef32_pk_fp4_f32 v184, v42, v43, 1.0 op_sel:[0,0,1,0]
	v_cvt_scalef32_pk_fp4_f32 v185, v58, v59, 1.0 op_sel:[0,0,1,0]
	v_cvt_scalef32_pk_fp4_f32 v184, v44, v45, 1.0 op_sel:[0,0,0,1]
	v_cvt_scalef32_pk_fp4_f32 v185, v60, v61, 1.0 op_sel:[0,0,0,1]
	v_cvt_scalef32_pk_fp4_f32 v184, v46, v47, 1.0 op_sel:[0,0,1,1]
	v_cvt_scalef32_pk_fp4_f32 v185, v62, v63, 1.0 op_sel:[0,0,1,1]
	s_waitcnt lgkmcnt(2)
	v_cmp_lt_i32_e32 vcc, -1, v177
	v_lshl_add_u32 v181, v177, 9, v180
	s_and_saveexec_b64 s[50:51], vcc
	global_store_dwordx2 v181, v[184:185], s[48:49]
	s_or_b64 exec, exec, s[50:51]
	v_cvt_scalef32_pk_fp4_f32 v182, v16, v17, 1.0
	v_cvt_scalef32_pk_fp4_f32 v183, v24, v25, 1.0
	v_cvt_scalef32_pk_fp4_f32 v182, v18, v19, 1.0 op_sel:[0,0,1,0]
	v_cvt_scalef32_pk_fp4_f32 v183, v26, v27, 1.0 op_sel:[0,0,1,0]
	v_cvt_scalef32_pk_fp4_f32 v182, v20, v21, 1.0 op_sel:[0,0,0,1]
	v_cvt_scalef32_pk_fp4_f32 v183, v28, v29, 1.0 op_sel:[0,0,0,1]
	v_cvt_scalef32_pk_fp4_f32 v182, v22, v23, 1.0 op_sel:[0,0,1,1]
	v_cvt_scalef32_pk_fp4_f32 v183, v30, v31, 1.0 op_sel:[0,0,1,1]
	s_waitcnt lgkmcnt(1)
	v_cmp_lt_i32_e32 vcc, -1, v178
	v_lshl_add_u32 v181, v178, 9, v180
	s_and_saveexec_b64 s[50:51], vcc
	global_store_dwordx2 v181, v[182:183], s[48:49]
	s_or_b64 exec, exec, s[50:51]
	v_cvt_scalef32_pk_fp4_f32 v184, v4, v5, 1.0
	v_cvt_scalef32_pk_fp4_f32 v185, v12, v13, 1.0
	v_cvt_scalef32_pk_fp4_f32 v184, v6, v7, 1.0 op_sel:[0,0,1,0]
	v_cvt_scalef32_pk_fp4_f32 v185, v14, v15, 1.0 op_sel:[0,0,1,0]
	v_cvt_scalef32_pk_fp4_f32 v184, v8, v9, 1.0 op_sel:[0,0,0,1]
	v_cvt_scalef32_pk_fp4_f32 v185, v0, v1, 1.0 op_sel:[0,0,0,1]
	v_cvt_scalef32_pk_fp4_f32 v184, v10, v11, 1.0 op_sel:[0,0,1,1]
	v_cvt_scalef32_pk_fp4_f32 v185, v2, v3, 1.0 op_sel:[0,0,1,1]
	s_waitcnt lgkmcnt(0)
	v_cmp_lt_i32_e32 vcc, -1, v179
	v_lshl_add_u32 v181, v179, 9, v180
	s_and_saveexec_b64 s[50:51], vcc
	global_store_dwordx2 v181, v[184:185], s[48:49]
	s_or_b64 exec, exec, s[50:51]

; #define GAS __attribute__((address_space(1)))
;     __device__ __forceinline__ void operator()(const f32x4 (&acc)[2][2][4][2], const Unit& u, int wr, int wc, int fr, int fq, const Pre& pre, bool drain) const {
;     ...
;             u32x2 o[2][4];
; #pragma unroll
;             for (int ai = 0; ai < 2; ++ai)
; #pragma unroll
;                 for (int m = 0; m < 4; ++m) { unsigned w[2];
; #pragma unroll
;                     for (int bj = 0; bj < 2; ++bj) { const f32x4 v0 = acc[ai][bj][m][0], v1 = acc[ai][bj][m][1];
;                         unsigned x = 0u;
;                         x = __builtin_amdgcn_cvt_scalef32_pk_fp4_f32(x, v0[0], v0[1], 1.0f, 0); x = __builtin_amdgcn_cvt_scalef32_pk_fp4_f32(x, v0[2], v0[3], 1.0f, 1);
;                         x = __builtin_amdgcn_cvt_scalef32_pk_fp4_f32(x, v1[0], v1[1], 1.0f, 2); x = __builtin_amdgcn_cvt_scalef32_pk_fp4_f32(x, v1[2], v1[3], 1.0f, 3);
;                         w[bj] = x; }
;                     o[ai][m] = (u32x2){w[0], w[1]}; }
;             if (drain) asm volatile("s_waitcnt vmcnt(0)" ::: "memory");
; #pragma unroll
;             for (int ai = 0; ai < 2; ++ai)
; #pragma unroll
;                 for (int m = 0; m < 4; ++m) { const int dst = pre.tab[wr * 64 + fr + ai * HALF + m * 16];
;                     if (dst >= 0) *(GAS u32x2*)(Y2 + (size_t)dst * 512 + (u.ocol0 >> 1) + wc * 32 + fq * 8) = o[ai][m]; }
.LBB0_1597:
	s_or_b64 exec, exec, s[56:57]
	s_add_i32 s0, s4, s76
	v_lshl_add_u32 v139, v164, 2, s0
	v_ashrrev_i32_e32 v146, 1, v154
	v_ashrrev_i32_e32 v147, 31, v146
	ds_read_b32 v172, v139
	ds_read_b32 v173, v139 offset:64
	ds_read_b32 v174, v139 offset:128
	ds_read_b32 v175, v139 offset:192
	ds_read_b32 v176, v139 offset:512
	ds_read_b32 v177, v139 offset:576
	ds_read_b32 v178, v139 offset:640
	ds_read_b32 v179, v139 offset:704
	v_add_u32_e32 v180, s22, v146
	v_add_u32_e32 v180, v180, v142
	v_cvt_scalef32_pk_fp4_f32 v182, v116, v117, 1.0
	v_cvt_scalef32_pk_fp4_f32 v183, v124, v125, 1.0
	v_cvt_scalef32_pk_fp4_f32 v182, v118, v119, 1.0 op_sel:[0,0,1,0]
	v_cvt_scalef32_pk_fp4_f32 v183, v126, v127, 1.0 op_sel:[0,0,1,0]
	v_cvt_scalef32_pk_fp4_f32 v182, v112, v113, 1.0 op_sel:[0,0,0,1]
	v_cvt_scalef32_pk_fp4_f32 v183, v120, v121, 1.0 op_sel:[0,0,0,1]
	v_cvt_scalef32_pk_fp4_f32 v182, v114, v115, 1.0 op_sel:[0,0,1,1]
	v_cvt_scalef32_pk_fp4_f32 v183, v122, v123, 1.0 op_sel:[0,0,1,1]
	s_waitcnt lgkmcnt(7)
	v_cmp_lt_i32_e32 vcc, -1, v172
	v_lshl_add_u32 v181, v172, 9, v180
	s_and_saveexec_b64 s[56:57], vcc
	global_store_dwordx2 v181, v[182:183], s[48:49]
	s_or_b64 exec, exec, s[56:57]
	v_cvt_scalef32_pk_fp4_f32 v184, v100, v101, 1.0
	v_cvt_scalef32_pk_fp4_f32 v185, v108, v109, 1.0
	v_cvt_scalef32_pk_fp4_f32 v184, v102, v103, 1.0 op_sel:[0,0,1,0]
	v_cvt_scalef32_pk_fp4_f32 v185, v110, v111, 1.0 op_sel:[0,0,1,0]
	v_cvt_scalef32_pk_fp4_f32 v184, v96, v97, 1.0 op_sel:[0,0,0,1]
	v_cvt_scalef32_pk_fp4_f32 v185, v104, v105, 1.0 op_sel:[0,0,0,1]
	v_cvt_scalef32_pk_fp4_f32 v184, v98, v99, 1.0 op_sel:[0,0,1,1]
	v_cvt_scalef32_pk_fp4_f32 v185, v106, v107, 1.0 op_sel:[0,0,1,1]
	s_waitcnt lgkmcnt(6)
	v_cmp_lt_i32_e32 vcc, -1, v173
	v_lshl_add_u32 v181, v173, 9, v180
	s_and_saveexec_b64 s[56:57], vcc
	global_store_dwordx2 v181, v[184:185], s[48:49]
	s_or_b64 exec, exec, s[56:57]
	v_cvt_scalef32_pk_fp4_f32 v182, v84, v85, 1.0
	v_cvt_scalef32_pk_fp4_f32 v183, v92, v93, 1.0
	v_cvt_scalef32_pk_fp4_f32 v182, v86, v87, 1.0 op_sel:[0,0,1,0]
	v_cvt_scalef32_pk_fp4_f32 v183, v94, v95, 1.0 op_sel:[0,0,1,0]
	v_cvt_scalef32_pk_fp4_f32 v182, v80, v81, 1.0 op_sel:[0,0,0,1]
	v_cvt_scalef32_pk_fp4_f32 v183, v88, v89, 1.0 op_sel:[0,0,0,1]
	v_cvt_scalef32_pk_fp4_f32 v182, v82, v83, 1.0 op_sel:[0,0,1,1]
	v_cvt_scalef32_pk_fp4_f32 v183, v90, v91, 1.0 op_sel:[0,0,1,1]
	s_waitcnt lgkmcnt(5)
	v_cmp_lt_i32_e32 vcc, -1, v174
	v_lshl_add_u32 v181, v174, 9, v180
	s_and_saveexec_b64 s[56:57], vcc
	global_store_dwordx2 v181, v[182:183], s[48:49]
	s_or_b64 exec, exec, s[56:57]
	v_cvt_scalef32_pk_fp4_f32 v184, v52, v53, 1.0
	v_cvt_scalef32_pk_fp4_f32 v185, v60, v61, 1.0
	v_cvt_scalef32_pk_fp4_f32 v184, v54, v55, 1.0 op_sel:[0,0,1,0]
	v_cvt_scalef32_pk_fp4_f32 v185, v62, v63, 1.0 op_sel:[0,0,1,0]
	v_cvt_scalef32_pk_fp4_f32 v184, v48, v49, 1.0 op_sel:[0,0,0,1]
	v_cvt_scalef32_pk_fp4_f32 v185, v56, v57, 1.0 op_sel:[0,0,0,1]
	v_cvt_scalef32_pk_fp4_f32 v184, v50, v51, 1.0 op_sel:[0,0,1,1]
	v_cvt_scalef32_pk_fp4_f32 v185, v58, v59, 1.0 op_sel:[0,0,1,1]
	s_waitcnt lgkmcnt(4)
	v_cmp_lt_i32_e32 vcc, -1, v175
	v_lshl_add_u32 v181, v175, 9, v180
	s_and_saveexec_b64 s[56:57], vcc
	global_store_dwordx2 v181, v[184:185], s[48:49]
	s_or_b64 exec, exec, s[56:57]
	v_cvt_scalef32_pk_fp4_f32 v182, v68, v69, 1.0
	v_cvt_scalef32_pk_fp4_f32 v183, v76, v77, 1.0
	v_cvt_scalef32_pk_fp4_f32 v182, v70, v71, 1.0 op_sel:[0,0,1,0]
	v_cvt_scalef32_pk_fp4_f32 v183, v78, v79, 1.0 op_sel:[0,0,1,0]
	v_cvt_scalef32_pk_fp4_f32 v182, v64, v65, 1.0 op_sel:[0,0,0,1]
	v_cvt_scalef32_pk_fp4_f32 v183, v72, v73, 1.0 op_sel:[0,0,0,1]
	v_cvt_scalef32_pk_fp4_f32 v182, v66, v67, 1.0 op_sel:[0,0,1,1]
	v_cvt_scalef32_pk_fp4_f32 v183, v74, v75, 1.0 op_sel:[0,0,1,1]
	s_waitcnt lgkmcnt(3)
	v_cmp_lt_i32_e32 vcc, -1, v176
	v_lshl_add_u32 v181, v176, 9, v180
	s_and_saveexec_b64 s[56:57], vcc
	global_store_dwordx2 v181, v[182:183], s[48:49]
	s_or_b64 exec, exec, s[56:57]
	v_cvt_scalef32_pk_fp4_f32 v184, v36, v37, 1.0
	v_cvt_scalef32_pk_fp4_f32 v185, v44, v45, 1.0
	v_cvt_scalef32_pk_fp4_f32 v184, v38, v39, 1.0 op_sel:[0,0,1,0]
	v_cvt_scalef32_pk_fp4_f32 v185, v46, v47, 1.0 op_sel:[0,0,1,0]
	v_cvt_scalef32_pk_fp4_f32 v184, v32, v33, 1.0 op_sel:[0,0,0,1]
	v_cvt_scalef32_pk_fp4_f32 v185, v40, v41, 1.0 op_sel:[0,0,0,1]
	v_cvt_scalef32_pk_fp4_f32 v184, v34, v35, 1.0 op_sel:[0,0,1,1]
	v_cvt_scalef32_pk_fp4_f32 v185, v42, v43, 1.0 op_sel:[0,0,1,1]
	s_waitcnt lgkmcnt(2)
	v_cmp_lt_i32_e32 vcc, -1, v177
	v_lshl_add_u32 v181, v177, 9, v180
	s_and_saveexec_b64 s[56:57], vcc
	global_store_dwordx2 v181, v[184:185], s[48:49]
	s_or_b64 exec, exec, s[56:57]
	v_cvt_scalef32_pk_fp4_f32 v182, v20, v21, 1.0
	v_cvt_scalef32_pk_fp4_f32 v183, v28, v29, 1.0
	v_cvt_scalef32_pk_fp4_f32 v182, v22, v23, 1.0 op_sel:[0,0,1,0]
	v_cvt_scalef32_pk_fp4_f32 v183, v30, v31, 1.0 op_sel:[0,0,1,0]
	v_cvt_scalef32_pk_fp4_f32 v182, v16, v17, 1.0 op_sel:[0,0,0,1]
	v_cvt_scalef32_pk_fp4_f32 v183, v24, v25, 1.0 op_sel:[0,0,0,1]
	v_cvt_scalef32_pk_fp4_f32 v182, v18, v19, 1.0 op_sel:[0,0,1,1]
	v_cvt_scalef32_pk_fp4_f32 v183, v26, v27, 1.0 op_sel:[0,0,1,1]
	s_waitcnt lgkmcnt(1)
	v_cmp_lt_i32_e32 vcc, -1, v178
	v_lshl_add_u32 v181, v178, 9, v180
	s_and_saveexec_b64 s[56:57], vcc
	global_store_dwordx2 v181, v[182:183], s[48:49]
	s_or_b64 exec, exec, s[56:57]
	v_cvt_scalef32_pk_fp4_f32 v184, v8, v9, 1.0
	v_cvt_scalef32_pk_fp4_f32 v185, v12, v13, 1.0
	v_cvt_scalef32_pk_fp4_f32 v184, v10, v11, 1.0 op_sel:[0,0,1,0]
	v_cvt_scalef32_pk_fp4_f32 v185, v14, v15, 1.0 op_sel:[0,0,1,0]
	v_cvt_scalef32_pk_fp4_f32 v184, v4, v5, 1.0 op_sel:[0,0,0,1]
	v_cvt_scalef32_pk_fp4_f32 v185, v0, v1, 1.0 op_sel:[0,0,0,1]
	v_cvt_scalef32_pk_fp4_f32 v184, v6, v7, 1.0 op_sel:[0,0,1,1]
	v_cvt_scalef32_pk_fp4_f32 v185, v2, v3, 1.0 op_sel:[0,0,1,1]
	s_waitcnt lgkmcnt(0)
	v_cmp_lt_i32_e32 vcc, -1, v179
	v_lshl_add_u32 v181, v179, 9, v180
	s_and_saveexec_b64 s[56:57], vcc
	global_store_dwordx2 v181, v[184:185], s[48:49]
	s_or_b64 exec, exec, s[56:57]
